# K-loops: first iteration peeled, first MFMA of each accumulator takes C=0, accumulator clearing removed
# speedup vs baseline: 1.0096x; 1.0096x over previous
.LBB0_163:
	s_ashr_i32 s31, s30, 31
	s_lshl_b64 s[36:37], s[30:31], 19
	s_add_u32 s36, s44, s36
	s_addc_u32 s37, s45, s37
	s_and_b64 s[38:39], s[4:5], exec
	s_cselect_b32 s11, s37, s13
	s_cselect_b32 s31, s36, s12
	s_ashr_i32 s35, s34, 31
	s_lshl_b64 s[38:39], s[34:35], 19
	s_add_u32 s38, s46, s38
	s_addc_u32 s39, s47, s39
	s_and_b64 s[40:41], s[4:5], exec
	s_cselect_b32 s35, s39, s15
	s_cselect_b32 s64, s38, s14
	s_add_u32 s65, s14, 0x100
	s_addc_u32 s66, s15, 0
	s_mov_b32 s67, -2
.Lpk0_entry:
	s_waitcnt lgkmcnt(0)
	ds_read_b128 v[106:109], v198
	ds_read_b128 v[110:113], v198 offset:1024
	ds_read_b128 v[114:117], v198 offset:2048
	ds_read_b128 v[118:121], v198 offset:3072
	ds_read_b128 v[182:185], v199
	ds_read_b128 v[186:189], v199 offset:1024
	ds_read_b128 v[190:193], v199 offset:2048
	ds_read_b128 v[202:205], v199 offset:3072
	s_add_u32 s14, s12, 0x100
	s_addc_u32 s15, s13, 0
	s_cmp_eq_u32 s67, 12
	s_cselect_b32 s43, s11, s15
	s_cselect_b32 s42, s31, s14
	s_cselect_b32 s41, s35, s66
	s_cselect_b32 s40, s64, s65
	v_lshl_add_u64 v[194:195], s[12:13], 0, v[172:173]
	s_add_i32 m0, s53, 0xc000
	ds_read_b128 v[206:209], v200
	ds_read_b128 v[210:213], v200 offset:1024
	ds_read_b128 v[214:217], v200 offset:2048
	ds_read_b128 v[218:221], v200 offset:3072
	ds_read_b128 v[222:225], v200 offset:4096
	ds_read_b128 v[226:229], v200 offset:5120
	ds_read_b128 v[230:233], v200 offset:6144
	ds_read_b128 v[234:237], v200 offset:7168
	global_load_lds_dwordx4 v[194:195], off
	v_lshl_add_u64 v[194:195], s[12:13], 0, v[174:175]
	s_add_i32 m0, s53, 0xe000
	s_nop 0
	global_load_lds_dwordx4 v[194:195], off
	s_waitcnt vmcnt(8)
	s_waitcnt lgkmcnt(0)
	s_barrier
	s_setprio 1
	s_waitcnt lgkmcnt(0)
	v_mfma_i32_16x16x64_i8 v[142:145], v[106:109], v[206:209], 0
	v_mfma_i32_16x16x64_i8 v[138:141], v[114:117], v[206:209], 0
	v_mfma_i32_16x16x64_i8 v[122:125], v[106:109], v[214:217], 0
	v_mfma_i32_16x16x64_i8 v[126:129], v[114:117], v[214:217], 0
	v_mfma_i32_16x16x64_i8 v[94:97], v[106:109], v[222:225], 0
	v_mfma_i32_16x16x64_i8 v[90:93], v[114:117], v[222:225], 0
	v_mfma_i32_16x16x64_i8 v[74:77], v[106:109], v[230:233], 0
	v_mfma_i32_16x16x64_i8 v[82:85], v[114:117], v[230:233], 0
	v_mfma_i32_16x16x64_i8 v[142:145], v[110:113], v[210:213], v[142:145]
	v_mfma_i32_16x16x64_i8 v[138:141], v[118:121], v[210:213], v[138:141]
	v_mfma_i32_16x16x64_i8 v[122:125], v[110:113], v[218:221], v[122:125]
	v_mfma_i32_16x16x64_i8 v[126:129], v[118:121], v[218:221], v[126:129]
	v_mfma_i32_16x16x64_i8 v[94:97], v[110:113], v[226:229], v[94:97]
	v_mfma_i32_16x16x64_i8 v[90:93], v[118:121], v[226:229], v[90:93]
	v_mfma_i32_16x16x64_i8 v[74:77], v[110:113], v[234:237], v[74:77]
	v_mfma_i32_16x16x64_i8 v[82:85], v[118:121], v[234:237], v[82:85]
	s_setprio 0
	s_setprio 1
	v_mfma_i32_16x16x64_i8 v[134:137], v[182:185], v[206:209], 0
	v_mfma_i32_16x16x64_i8 v[130:133], v[190:193], v[206:209], 0
	v_mfma_i32_16x16x64_i8 v[98:101], v[182:185], v[214:217], 0
	v_mfma_i32_16x16x64_i8 v[102:105], v[190:193], v[214:217], 0
	v_mfma_i32_16x16x64_i8 v[86:89], v[182:185], v[222:225], 0
	v_mfma_i32_16x16x64_i8 v[78:81], v[190:193], v[222:225], 0
	v_mfma_i32_16x16x64_i8 v[58:61], v[182:185], v[230:233], 0
	v_mfma_i32_16x16x64_i8 v[70:73], v[190:193], v[230:233], 0
	v_mfma_i32_16x16x64_i8 v[134:137], v[186:189], v[210:213], v[134:137]
	v_mfma_i32_16x16x64_i8 v[130:133], v[202:205], v[210:213], v[130:133]
	v_mfma_i32_16x16x64_i8 v[98:101], v[186:189], v[218:221], v[98:101]
	v_mfma_i32_16x16x64_i8 v[102:105], v[202:205], v[218:221], v[102:105]
	v_mfma_i32_16x16x64_i8 v[86:89], v[186:189], v[226:229], v[86:89]
	v_mfma_i32_16x16x64_i8 v[78:81], v[202:205], v[226:229], v[78:81]
	v_mfma_i32_16x16x64_i8 v[58:61], v[186:189], v[234:237], v[58:61]
	v_mfma_i32_16x16x64_i8 v[70:73], v[202:205], v[234:237], v[70:73]
	s_setprio 0
	s_barrier
	s_add_i32 s12, s60, s29
	v_lshl_add_u64 v[194:195], s[40:41], 0, v[148:149]
	s_mov_b32 m0, s12
	ds_read_b128 v[206:209], v200 offset:16384
	ds_read_b128 v[210:213], v200 offset:17408
	ds_read_b128 v[214:217], v200 offset:18432
	ds_read_b128 v[218:221], v200 offset:19456
	ds_read_b128 v[222:225], v200 offset:20480
	ds_read_b128 v[226:229], v200 offset:21504
	ds_read_b128 v[230:233], v200 offset:22528
	ds_read_b128 v[234:237], v200 offset:23552
	global_load_lds_dwordx4 v[194:195], off
	s_add_i32 m0, s12, 0x2000
	s_add_u32 s12, s40, 0x40000
	v_lshl_add_u64 v[238:239], s[40:41], 0, v[150:151]
	s_addc_u32 s13, s41, 0
	s_add_i32 s68, s61, s29
	global_load_lds_dwordx4 v[238:239], off
	v_lshl_add_u64 v[240:241], s[12:13], 0, v[148:149]
	s_mov_b32 m0, s68
	v_lshl_add_u64 v[242:243], s[42:43], 0, v[154:155]
	global_load_lds_dwordx4 v[240:241], off
	v_lshl_add_u64 v[240:241], s[12:13], 0, v[150:151]
	s_add_i32 m0, s68, 0x2000
	s_nop 0
	global_load_lds_dwordx4 v[240:241], off
	v_lshl_add_u64 v[240:241], s[42:43], 0, v[152:153]
	s_mov_b32 m0, s53
	s_nop 0
	global_load_lds_dwordx4 v[240:241], off
	s_mov_b32 m0, s54
	s_nop 0
	global_load_lds_dwordx4 v[242:243], off
	s_waitcnt vmcnt(8)
	s_waitcnt lgkmcnt(0)
	s_barrier
	s_setprio 1
	s_waitcnt lgkmcnt(0)
	v_mfma_i32_16x16x64_i8 v[54:57], v[106:109], v[206:209], 0
	v_mfma_i32_16x16x64_i8 v[50:53], v[114:117], v[206:209], 0
	v_mfma_i32_16x16x64_i8 v[34:37], v[106:109], v[214:217], 0
	v_mfma_i32_16x16x64_i8 v[38:41], v[114:117], v[214:217], 0
	v_mfma_i32_16x16x64_i8 v[22:25], v[106:109], v[222:225], 0
	v_mfma_i32_16x16x64_i8 v[18:21], v[114:117], v[222:225], 0
	v_mfma_i32_16x16x64_i8 v[2:5], v[106:109], v[230:233], 0
	v_mfma_i32_16x16x64_i8 v[6:9], v[114:117], v[230:233], 0
	v_mfma_i32_16x16x64_i8 v[54:57], v[110:113], v[210:213], v[54:57]
	v_mfma_i32_16x16x64_i8 v[50:53], v[118:121], v[210:213], v[50:53]
	v_mfma_i32_16x16x64_i8 v[34:37], v[110:113], v[218:221], v[34:37]
	v_mfma_i32_16x16x64_i8 v[38:41], v[118:121], v[218:221], v[38:41]
	v_mfma_i32_16x16x64_i8 v[22:25], v[110:113], v[226:229], v[22:25]
	v_mfma_i32_16x16x64_i8 v[18:21], v[118:121], v[226:229], v[18:21]
	v_mfma_i32_16x16x64_i8 v[2:5], v[110:113], v[234:237], v[2:5]
	v_mfma_i32_16x16x64_i8 v[6:9], v[118:121], v[234:237], v[6:9]
	s_setprio 0
	s_setprio 1
	v_mfma_i32_16x16x64_i8 v[66:69], v[182:185], v[206:209], 0
	v_mfma_i32_16x16x64_i8 v[62:65], v[190:193], v[206:209], 0
	v_mfma_i32_16x16x64_i8 v[42:45], v[182:185], v[214:217], 0
	v_mfma_i32_16x16x64_i8 v[46:49], v[190:193], v[214:217], 0
	v_mfma_i32_16x16x64_i8 v[30:33], v[182:185], v[222:225], 0
	v_mfma_i32_16x16x64_i8 v[26:29], v[190:193], v[222:225], 0
	v_mfma_i32_16x16x64_i8 v[10:13], v[182:185], v[230:233], 0
	v_mfma_i32_16x16x64_i8 v[14:17], v[190:193], v[230:233], 0
	v_mfma_i32_16x16x64_i8 v[66:69], v[186:189], v[210:213], v[66:69]
	v_mfma_i32_16x16x64_i8 v[62:65], v[202:205], v[210:213], v[62:65]
	v_mfma_i32_16x16x64_i8 v[42:45], v[186:189], v[218:221], v[42:45]
	v_mfma_i32_16x16x64_i8 v[46:49], v[202:205], v[218:221], v[46:49]
	v_mfma_i32_16x16x64_i8 v[30:33], v[186:189], v[226:229], v[30:33]
	v_mfma_i32_16x16x64_i8 v[26:29], v[202:205], v[226:229], v[26:29]
	v_mfma_i32_16x16x64_i8 v[10:13], v[186:189], v[234:237], v[10:13]
	v_mfma_i32_16x16x64_i8 v[14:17], v[202:205], v[234:237], v[14:17]
	s_setprio 0
	s_barrier
	s_add_i32 s12, 0, 0x18000
	s_add_i32 s68, 0, 0x1c000
	v_add_u32_e32 v118, s12, v196
	v_add_u32_e32 v146, s68, v196
	ds_read_b128 v[106:109], v118
	ds_read_b128 v[110:113], v118 offset:1024
	ds_read_b128 v[114:117], v118 offset:2048
	ds_read_b128 v[118:121], v118 offset:3072
	ds_read_b128 v[182:185], v146
	ds_read_b128 v[186:189], v146 offset:1024
	ds_read_b128 v[190:193], v146 offset:2048
	ds_read_b128 v[202:205], v146 offset:3072
	s_mov_b32 m0, s55
	v_lshl_add_u64 v[244:245], s[42:43], 0, v[156:157]
	ds_read_b128 v[206:209], v200 offset:32768
	ds_read_b128 v[210:213], v200 offset:33792
	ds_read_b128 v[214:217], v200 offset:34816
	ds_read_b128 v[218:221], v200 offset:35840
	ds_read_b128 v[222:225], v200 offset:36864
	ds_read_b128 v[226:229], v200 offset:37888
	ds_read_b128 v[230:233], v200 offset:38912
	ds_read_b128 v[234:237], v200 offset:39936
	global_load_lds_dwordx4 v[244:245], off
	v_lshl_add_u64 v[244:245], s[42:43], 0, v[158:159]
	s_mov_b32 m0, s56
	s_nop 0
	global_load_lds_dwordx4 v[244:245], off
	s_waitcnt vmcnt(8)
	s_waitcnt lgkmcnt(0)
	s_barrier
	s_setprio 1
	s_waitcnt lgkmcnt(0)
	v_mfma_i32_16x16x64_i8 v[142:145], v[106:109], v[206:209], v[142:145]
	v_mfma_i32_16x16x64_i8 v[138:141], v[114:117], v[206:209], v[138:141]
	v_mfma_i32_16x16x64_i8 v[122:125], v[106:109], v[214:217], v[122:125]
	v_mfma_i32_16x16x64_i8 v[126:129], v[114:117], v[214:217], v[126:129]
	v_mfma_i32_16x16x64_i8 v[94:97], v[106:109], v[222:225], v[94:97]
	v_mfma_i32_16x16x64_i8 v[90:93], v[114:117], v[222:225], v[90:93]
	v_mfma_i32_16x16x64_i8 v[74:77], v[106:109], v[230:233], v[74:77]
	v_mfma_i32_16x16x64_i8 v[82:85], v[114:117], v[230:233], v[82:85]
	v_mfma_i32_16x16x64_i8 v[142:145], v[110:113], v[210:213], v[142:145]
	v_mfma_i32_16x16x64_i8 v[138:141], v[118:121], v[210:213], v[138:141]
	v_mfma_i32_16x16x64_i8 v[122:125], v[110:113], v[218:221], v[122:125]
	v_mfma_i32_16x16x64_i8 v[126:129], v[118:121], v[218:221], v[126:129]
	v_mfma_i32_16x16x64_i8 v[94:97], v[110:113], v[226:229], v[94:97]
	v_mfma_i32_16x16x64_i8 v[90:93], v[118:121], v[226:229], v[90:93]
	v_mfma_i32_16x16x64_i8 v[74:77], v[110:113], v[234:237], v[74:77]
	v_mfma_i32_16x16x64_i8 v[82:85], v[118:121], v[234:237], v[82:85]
	s_setprio 0
	s_setprio 1
	v_mfma_i32_16x16x64_i8 v[134:137], v[182:185], v[206:209], v[134:137]
	v_mfma_i32_16x16x64_i8 v[130:133], v[190:193], v[206:209], v[130:133]
	v_mfma_i32_16x16x64_i8 v[98:101], v[182:185], v[214:217], v[98:101]
	v_mfma_i32_16x16x64_i8 v[102:105], v[190:193], v[214:217], v[102:105]
	v_mfma_i32_16x16x64_i8 v[86:89], v[182:185], v[222:225], v[86:89]
	v_mfma_i32_16x16x64_i8 v[78:81], v[190:193], v[222:225], v[78:81]
	v_mfma_i32_16x16x64_i8 v[58:61], v[182:185], v[230:233], v[58:61]
	v_mfma_i32_16x16x64_i8 v[70:73], v[190:193], v[230:233], v[70:73]
	v_mfma_i32_16x16x64_i8 v[134:137], v[186:189], v[210:213], v[134:137]
	v_mfma_i32_16x16x64_i8 v[130:133], v[202:205], v[210:213], v[130:133]
	v_mfma_i32_16x16x64_i8 v[98:101], v[186:189], v[218:221], v[98:101]
	v_mfma_i32_16x16x64_i8 v[102:105], v[202:205], v[218:221], v[102:105]
	v_mfma_i32_16x16x64_i8 v[86:89], v[186:189], v[226:229], v[86:89]
	v_mfma_i32_16x16x64_i8 v[78:81], v[202:205], v[226:229], v[78:81]
	v_mfma_i32_16x16x64_i8 v[58:61], v[186:189], v[234:237], v[58:61]
	v_mfma_i32_16x16x64_i8 v[70:73], v[202:205], v[234:237], v[70:73]
	s_setprio 0
	s_barrier
	s_add_i32 s12, s12, s29
	v_lshl_add_u64 v[194:195], v[194:195], 0, s[24:25]
	s_mov_b32 m0, s12
	ds_read_b128 v[206:209], v200 offset:49152
	ds_read_b128 v[210:213], v200 offset:50176
	ds_read_b128 v[214:217], v200 offset:51200
	ds_read_b128 v[218:221], v200 offset:52224
	ds_read_b128 v[222:225], v200 offset:53248
	ds_read_b128 v[226:229], v200 offset:54272
	ds_read_b128 v[230:233], v200 offset:55296
	ds_read_b128 v[234:237], v200 offset:56320
	global_load_lds_dwordx4 v[194:195], off
	s_add_i32 m0, s12, 0x2000
	s_add_u32 s12, s40, 0x40080
	v_lshl_add_u64 v[194:195], v[238:239], 0, s[24:25]
	s_addc_u32 s13, s41, 0
	s_add_i32 s40, s68, s29
	global_load_lds_dwordx4 v[194:195], off
	v_lshl_add_u64 v[194:195], s[12:13], 0, v[148:149]
	s_mov_b32 m0, s40
	s_nop 0
	global_load_lds_dwordx4 v[194:195], off
	v_lshl_add_u64 v[194:195], s[12:13], 0, v[150:151]
	s_add_i32 m0, s40, 0x2000
	s_nop 0
	global_load_lds_dwordx4 v[194:195], off
	v_lshl_add_u64 v[194:195], v[240:241], 0, s[24:25]
	s_mov_b32 m0, s58
	s_nop 0
	global_load_lds_dwordx4 v[194:195], off
	v_lshl_add_u64 v[194:195], v[242:243], 0, s[24:25]
	s_mov_b32 m0, s59
	s_nop 0
	global_load_lds_dwordx4 v[194:195], off
	s_waitcnt vmcnt(8)
	s_waitcnt lgkmcnt(0)
	s_barrier
	s_setprio 1
	s_waitcnt lgkmcnt(0)
	v_mfma_i32_16x16x64_i8 v[54:57], v[106:109], v[206:209], v[54:57]
	v_mfma_i32_16x16x64_i8 v[50:53], v[114:117], v[206:209], v[50:53]
	v_mfma_i32_16x16x64_i8 v[34:37], v[106:109], v[214:217], v[34:37]
	v_mfma_i32_16x16x64_i8 v[38:41], v[114:117], v[214:217], v[38:41]
	v_mfma_i32_16x16x64_i8 v[22:25], v[106:109], v[222:225], v[22:25]
	v_mfma_i32_16x16x64_i8 v[18:21], v[114:117], v[222:225], v[18:21]
	v_mfma_i32_16x16x64_i8 v[2:5], v[106:109], v[230:233], v[2:5]
	v_mfma_i32_16x16x64_i8 v[6:9], v[114:117], v[230:233], v[6:9]
	v_mfma_i32_16x16x64_i8 v[54:57], v[110:113], v[210:213], v[54:57]
	v_mfma_i32_16x16x64_i8 v[50:53], v[118:121], v[210:213], v[50:53]
	v_mfma_i32_16x16x64_i8 v[34:37], v[110:113], v[218:221], v[34:37]
	v_mfma_i32_16x16x64_i8 v[38:41], v[118:121], v[218:221], v[38:41]
	v_mfma_i32_16x16x64_i8 v[22:25], v[110:113], v[226:229], v[22:25]
	v_mfma_i32_16x16x64_i8 v[18:21], v[118:121], v[226:229], v[18:21]
	v_mfma_i32_16x16x64_i8 v[2:5], v[110:113], v[234:237], v[2:5]
	v_mfma_i32_16x16x64_i8 v[6:9], v[118:121], v[234:237], v[6:9]
	s_setprio 0
	s_setprio 1
	v_mfma_i32_16x16x64_i8 v[66:69], v[182:185], v[206:209], v[66:69]
	v_mfma_i32_16x16x64_i8 v[62:65], v[190:193], v[206:209], v[62:65]
	v_mfma_i32_16x16x64_i8 v[42:45], v[182:185], v[214:217], v[42:45]
	v_mfma_i32_16x16x64_i8 v[46:49], v[190:193], v[214:217], v[46:49]
	v_mfma_i32_16x16x64_i8 v[30:33], v[182:185], v[222:225], v[30:33]
	v_mfma_i32_16x16x64_i8 v[26:29], v[190:193], v[222:225], v[26:29]
	v_mfma_i32_16x16x64_i8 v[10:13], v[182:185], v[230:233], v[10:13]
	v_mfma_i32_16x16x64_i8 v[14:17], v[190:193], v[230:233], v[14:17]
	v_mfma_i32_16x16x64_i8 v[66:69], v[186:189], v[210:213], v[66:69]
	v_mfma_i32_16x16x64_i8 v[62:65], v[202:205], v[210:213], v[62:65]
	v_mfma_i32_16x16x64_i8 v[42:45], v[186:189], v[218:221], v[42:45]
	v_mfma_i32_16x16x64_i8 v[46:49], v[202:205], v[218:221], v[46:49]
	v_mfma_i32_16x16x64_i8 v[30:33], v[186:189], v[226:229], v[30:33]
	v_mfma_i32_16x16x64_i8 v[26:29], v[202:205], v[226:229], v[26:29]
	v_mfma_i32_16x16x64_i8 v[10:13], v[186:189], v[234:237], v[10:13]
	v_mfma_i32_16x16x64_i8 v[14:17], v[202:205], v[234:237], v[14:17]
	s_setprio 0
	s_barrier
	s_add_i32 s67, s67, 2
	s_add_u32 s65, s65, 0x100
	s_addc_u32 s66, s66, 0
	s_cmp_gt_u32 s67, 13
	s_mov_b64 s[12:13], s[14:15]
	s_cbranch_scc0 .LBB0_164
	s_branch .Lpk0_exit

.Lpk0_exit:
	s_and_b64 vcc, exec, s[4:5]
	s_cbranch_vccz .LBB0_171
	s_and_saveexec_b64 s[4:5], s[6:7]
	s_xor_b64 s[4:5], exec, s[4:5]
	s_lshl_b32 s12, s34, 8
	s_ashr_i32 s13, s12, 31
	v_lshl_add_u64 v[106:107], s[12:13], 2, v[168:169]
	s_movk_i32 s12, 0xfc00
	s_mov_b32 s13, -1
	v_lshl_add_u64 v[106:107], v[106:107], 0, s[12:13]
	s_andn2_saveexec_b64 s[4:5], s[4:5]
	s_lshl_b32 s12, s30, 8
	s_ashr_i32 s13, s12, 31
	v_lshl_add_u64 v[106:107], s[12:13], 2, v[170:171]
	s_or_b64 exec, exec, s[4:5]
	s_lshl_b32 s4, s63, 11
	s_and_b32 s4, s4, 0x800
	s_add_i32 m0, s52, s4
	s_nop 0
	global_load_lds_dword v[106:107], off

.LBB0_245:
	s_ashr_i32 s19, s18, 31
	s_lshl_b64 s[30:31], s[18:19], 19
	s_add_u32 s30, s44, s30
	s_addc_u32 s31, s45, s31
	s_and_b64 s[34:35], s[4:5], exec
	s_cselect_b32 s11, s31, s13
	s_cselect_b32 s19, s30, s12
	s_ashr_i32 s29, s28, 31
	s_lshl_b64 s[34:35], s[28:29], 19
	s_add_u32 s34, s46, s34
	s_addc_u32 s35, s47, s35
	s_and_b64 s[36:37], s[4:5], exec
	s_cselect_b32 s29, s35, s15
	s_cselect_b32 s60, s34, s14
	s_add_u32 s61, s14, 0x100
	s_addc_u32 s62, s15, 0
	s_mov_b32 s63, -2
.Lpk1_entry:
	s_waitcnt lgkmcnt(0)
	ds_read_b128 v[106:109], v198
	ds_read_b128 v[110:113], v198 offset:1024
	ds_read_b128 v[114:117], v198 offset:2048
	ds_read_b128 v[118:121], v198 offset:3072
	ds_read_b128 v[182:185], v199
	ds_read_b128 v[186:189], v199 offset:1024
	ds_read_b128 v[190:193], v199 offset:2048
	ds_read_b128 v[202:205], v199 offset:3072
	s_add_u32 s14, s12, 0x100
	s_addc_u32 s15, s13, 0
	s_cmp_eq_u32 s63, 12
	s_cselect_b32 s39, s11, s15
	s_cselect_b32 s38, s19, s14
	s_cselect_b32 s37, s29, s62
	s_cselect_b32 s36, s60, s61
	v_lshl_add_u64 v[194:195], s[12:13], 0, v[172:173]
	s_add_i32 m0, s42, 0xc000
	ds_read_b128 v[206:209], v200
	ds_read_b128 v[210:213], v200 offset:1024
	ds_read_b128 v[214:217], v200 offset:2048
	ds_read_b128 v[218:221], v200 offset:3072
	ds_read_b128 v[222:225], v200 offset:4096
	ds_read_b128 v[226:229], v200 offset:5120
	ds_read_b128 v[230:233], v200 offset:6144
	ds_read_b128 v[234:237], v200 offset:7168
	global_load_lds_dwordx4 v[194:195], off
	v_lshl_add_u64 v[194:195], s[12:13], 0, v[174:175]
	s_add_i32 m0, s42, 0xe000
	s_nop 0
	global_load_lds_dwordx4 v[194:195], off
	s_waitcnt vmcnt(8)
	s_waitcnt lgkmcnt(0)
	s_barrier
	s_setprio 1
	s_waitcnt lgkmcnt(0)
	v_mfma_i32_16x16x64_i8 v[142:145], v[106:109], v[206:209], 0
	v_mfma_i32_16x16x64_i8 v[138:141], v[114:117], v[206:209], 0
	v_mfma_i32_16x16x64_i8 v[122:125], v[106:109], v[214:217], 0
	v_mfma_i32_16x16x64_i8 v[126:129], v[114:117], v[214:217], 0
	v_mfma_i32_16x16x64_i8 v[94:97], v[106:109], v[222:225], 0
	v_mfma_i32_16x16x64_i8 v[90:93], v[114:117], v[222:225], 0
	v_mfma_i32_16x16x64_i8 v[74:77], v[106:109], v[230:233], 0
	v_mfma_i32_16x16x64_i8 v[82:85], v[114:117], v[230:233], 0
	v_mfma_i32_16x16x64_i8 v[142:145], v[110:113], v[210:213], v[142:145]
	v_mfma_i32_16x16x64_i8 v[138:141], v[118:121], v[210:213], v[138:141]
	v_mfma_i32_16x16x64_i8 v[122:125], v[110:113], v[218:221], v[122:125]
	v_mfma_i32_16x16x64_i8 v[126:129], v[118:121], v[218:221], v[126:129]
	v_mfma_i32_16x16x64_i8 v[94:97], v[110:113], v[226:229], v[94:97]
	v_mfma_i32_16x16x64_i8 v[90:93], v[118:121], v[226:229], v[90:93]
	v_mfma_i32_16x16x64_i8 v[74:77], v[110:113], v[234:237], v[74:77]
	v_mfma_i32_16x16x64_i8 v[82:85], v[118:121], v[234:237], v[82:85]
	s_setprio 0
	s_setprio 1
	v_mfma_i32_16x16x64_i8 v[134:137], v[182:185], v[206:209], 0
	v_mfma_i32_16x16x64_i8 v[130:133], v[190:193], v[206:209], 0
	v_mfma_i32_16x16x64_i8 v[98:101], v[182:185], v[214:217], 0
	v_mfma_i32_16x16x64_i8 v[102:105], v[190:193], v[214:217], 0
	v_mfma_i32_16x16x64_i8 v[86:89], v[182:185], v[222:225], 0
	v_mfma_i32_16x16x64_i8 v[78:81], v[190:193], v[222:225], 0
	v_mfma_i32_16x16x64_i8 v[58:61], v[182:185], v[230:233], 0
	v_mfma_i32_16x16x64_i8 v[70:73], v[190:193], v[230:233], 0
	v_mfma_i32_16x16x64_i8 v[134:137], v[186:189], v[210:213], v[134:137]
	v_mfma_i32_16x16x64_i8 v[130:133], v[202:205], v[210:213], v[130:133]
	v_mfma_i32_16x16x64_i8 v[98:101], v[186:189], v[218:221], v[98:101]
	v_mfma_i32_16x16x64_i8 v[102:105], v[202:205], v[218:221], v[102:105]
	v_mfma_i32_16x16x64_i8 v[86:89], v[186:189], v[226:229], v[86:89]
	v_mfma_i32_16x16x64_i8 v[78:81], v[202:205], v[226:229], v[78:81]
	v_mfma_i32_16x16x64_i8 v[58:61], v[186:189], v[234:237], v[58:61]
	v_mfma_i32_16x16x64_i8 v[70:73], v[202:205], v[234:237], v[70:73]
	s_setprio 0
	s_barrier
	s_add_i32 s12, s17, s40
	v_lshl_add_u64 v[194:195], s[36:37], 0, v[148:149]
	s_mov_b32 m0, s12
	ds_read_b128 v[206:209], v200 offset:16384
	ds_read_b128 v[210:213], v200 offset:17408
	ds_read_b128 v[214:217], v200 offset:18432
	ds_read_b128 v[218:221], v200 offset:19456
	ds_read_b128 v[222:225], v200 offset:20480
	ds_read_b128 v[226:229], v200 offset:21504
	ds_read_b128 v[230:233], v200 offset:22528
	ds_read_b128 v[234:237], v200 offset:23552
	global_load_lds_dwordx4 v[194:195], off
	s_add_i32 m0, s12, 0x2000
	s_add_u32 s12, s36, 0x40000
	v_lshl_add_u64 v[238:239], s[36:37], 0, v[150:151]
	s_addc_u32 s13, s37, 0
	s_add_i32 s64, s57, s40
	global_load_lds_dwordx4 v[238:239], off
	v_lshl_add_u64 v[240:241], s[12:13], 0, v[148:149]
	s_mov_b32 m0, s64
	v_lshl_add_u64 v[242:243], s[38:39], 0, v[154:155]
	global_load_lds_dwordx4 v[240:241], off
	v_lshl_add_u64 v[240:241], s[12:13], 0, v[150:151]
	s_add_i32 m0, s64, 0x2000
	s_nop 0
	global_load_lds_dwordx4 v[240:241], off
	v_lshl_add_u64 v[240:241], s[38:39], 0, v[152:153]
	s_mov_b32 m0, s42
	s_nop 0
	global_load_lds_dwordx4 v[240:241], off
	s_mov_b32 m0, s43
	s_nop 0
	global_load_lds_dwordx4 v[242:243], off
	s_waitcnt vmcnt(8)
	s_waitcnt lgkmcnt(0)
	s_barrier
	s_setprio 1
	s_waitcnt lgkmcnt(0)
	v_mfma_i32_16x16x64_i8 v[54:57], v[106:109], v[206:209], 0
	v_mfma_i32_16x16x64_i8 v[50:53], v[114:117], v[206:209], 0
	v_mfma_i32_16x16x64_i8 v[34:37], v[106:109], v[214:217], 0
	v_mfma_i32_16x16x64_i8 v[38:41], v[114:117], v[214:217], 0
	v_mfma_i32_16x16x64_i8 v[22:25], v[106:109], v[222:225], 0
	v_mfma_i32_16x16x64_i8 v[18:21], v[114:117], v[222:225], 0
	v_mfma_i32_16x16x64_i8 v[2:5], v[106:109], v[230:233], 0
	v_mfma_i32_16x16x64_i8 v[6:9], v[114:117], v[230:233], 0
	v_mfma_i32_16x16x64_i8 v[54:57], v[110:113], v[210:213], v[54:57]
	v_mfma_i32_16x16x64_i8 v[50:53], v[118:121], v[210:213], v[50:53]
	v_mfma_i32_16x16x64_i8 v[34:37], v[110:113], v[218:221], v[34:37]
	v_mfma_i32_16x16x64_i8 v[38:41], v[118:121], v[218:221], v[38:41]
	v_mfma_i32_16x16x64_i8 v[22:25], v[110:113], v[226:229], v[22:25]
	v_mfma_i32_16x16x64_i8 v[18:21], v[118:121], v[226:229], v[18:21]
	v_mfma_i32_16x16x64_i8 v[2:5], v[110:113], v[234:237], v[2:5]
	v_mfma_i32_16x16x64_i8 v[6:9], v[118:121], v[234:237], v[6:9]
	s_setprio 0
	s_setprio 1
	v_mfma_i32_16x16x64_i8 v[66:69], v[182:185], v[206:209], 0
	v_mfma_i32_16x16x64_i8 v[62:65], v[190:193], v[206:209], 0
	v_mfma_i32_16x16x64_i8 v[42:45], v[182:185], v[214:217], 0
	v_mfma_i32_16x16x64_i8 v[46:49], v[190:193], v[214:217], 0
	v_mfma_i32_16x16x64_i8 v[30:33], v[182:185], v[222:225], 0
	v_mfma_i32_16x16x64_i8 v[26:29], v[190:193], v[222:225], 0
	v_mfma_i32_16x16x64_i8 v[10:13], v[182:185], v[230:233], 0
	v_mfma_i32_16x16x64_i8 v[14:17], v[190:193], v[230:233], 0
	v_mfma_i32_16x16x64_i8 v[66:69], v[186:189], v[210:213], v[66:69]
	v_mfma_i32_16x16x64_i8 v[62:65], v[202:205], v[210:213], v[62:65]
	v_mfma_i32_16x16x64_i8 v[42:45], v[186:189], v[218:221], v[42:45]
	v_mfma_i32_16x16x64_i8 v[46:49], v[202:205], v[218:221], v[46:49]
	v_mfma_i32_16x16x64_i8 v[30:33], v[186:189], v[226:229], v[30:33]
	v_mfma_i32_16x16x64_i8 v[26:29], v[202:205], v[226:229], v[26:29]
	v_mfma_i32_16x16x64_i8 v[10:13], v[186:189], v[234:237], v[10:13]
	v_mfma_i32_16x16x64_i8 v[14:17], v[202:205], v[234:237], v[14:17]
	s_setprio 0
	s_barrier
	s_add_i32 s12, 0, 0x18000
	s_add_i32 s64, 0, 0x1c000
	v_add_u32_e32 v118, s12, v196
	v_add_u32_e32 v146, s64, v196
	ds_read_b128 v[106:109], v118
	ds_read_b128 v[110:113], v118 offset:1024
	ds_read_b128 v[114:117], v118 offset:2048
	ds_read_b128 v[118:121], v118 offset:3072
	ds_read_b128 v[182:185], v146
	ds_read_b128 v[186:189], v146 offset:1024
	ds_read_b128 v[190:193], v146 offset:2048
	ds_read_b128 v[202:205], v146 offset:3072
	s_mov_b32 m0, s52
	v_lshl_add_u64 v[244:245], s[38:39], 0, v[156:157]
	ds_read_b128 v[206:209], v200 offset:32768
	ds_read_b128 v[210:213], v200 offset:33792
	ds_read_b128 v[214:217], v200 offset:34816
	ds_read_b128 v[218:221], v200 offset:35840
	ds_read_b128 v[222:225], v200 offset:36864
	ds_read_b128 v[226:229], v200 offset:37888
	ds_read_b128 v[230:233], v200 offset:38912
	ds_read_b128 v[234:237], v200 offset:39936
	global_load_lds_dwordx4 v[244:245], off
	v_lshl_add_u64 v[244:245], s[38:39], 0, v[158:159]
	s_mov_b32 m0, s53
	s_nop 0
	global_load_lds_dwordx4 v[244:245], off
	s_waitcnt vmcnt(8)
	s_waitcnt lgkmcnt(0)
	s_barrier
	s_setprio 1
	s_waitcnt lgkmcnt(0)
	v_mfma_i32_16x16x64_i8 v[142:145], v[106:109], v[206:209], v[142:145]
	v_mfma_i32_16x16x64_i8 v[138:141], v[114:117], v[206:209], v[138:141]
	v_mfma_i32_16x16x64_i8 v[122:125], v[106:109], v[214:217], v[122:125]
	v_mfma_i32_16x16x64_i8 v[126:129], v[114:117], v[214:217], v[126:129]
	v_mfma_i32_16x16x64_i8 v[94:97], v[106:109], v[222:225], v[94:97]
	v_mfma_i32_16x16x64_i8 v[90:93], v[114:117], v[222:225], v[90:93]
	v_mfma_i32_16x16x64_i8 v[74:77], v[106:109], v[230:233], v[74:77]
	v_mfma_i32_16x16x64_i8 v[82:85], v[114:117], v[230:233], v[82:85]
	v_mfma_i32_16x16x64_i8 v[142:145], v[110:113], v[210:213], v[142:145]
	v_mfma_i32_16x16x64_i8 v[138:141], v[118:121], v[210:213], v[138:141]
	v_mfma_i32_16x16x64_i8 v[122:125], v[110:113], v[218:221], v[122:125]
	v_mfma_i32_16x16x64_i8 v[126:129], v[118:121], v[218:221], v[126:129]
	v_mfma_i32_16x16x64_i8 v[94:97], v[110:113], v[226:229], v[94:97]
	v_mfma_i32_16x16x64_i8 v[90:93], v[118:121], v[226:229], v[90:93]
	v_mfma_i32_16x16x64_i8 v[74:77], v[110:113], v[234:237], v[74:77]
	v_mfma_i32_16x16x64_i8 v[82:85], v[118:121], v[234:237], v[82:85]
	s_setprio 0
	s_setprio 1
	v_mfma_i32_16x16x64_i8 v[134:137], v[182:185], v[206:209], v[134:137]
	v_mfma_i32_16x16x64_i8 v[130:133], v[190:193], v[206:209], v[130:133]
	v_mfma_i32_16x16x64_i8 v[98:101], v[182:185], v[214:217], v[98:101]
	v_mfma_i32_16x16x64_i8 v[102:105], v[190:193], v[214:217], v[102:105]
	v_mfma_i32_16x16x64_i8 v[86:89], v[182:185], v[222:225], v[86:89]
	v_mfma_i32_16x16x64_i8 v[78:81], v[190:193], v[222:225], v[78:81]
	v_mfma_i32_16x16x64_i8 v[58:61], v[182:185], v[230:233], v[58:61]
	v_mfma_i32_16x16x64_i8 v[70:73], v[190:193], v[230:233], v[70:73]
	v_mfma_i32_16x16x64_i8 v[134:137], v[186:189], v[210:213], v[134:137]
	v_mfma_i32_16x16x64_i8 v[130:133], v[202:205], v[210:213], v[130:133]
	v_mfma_i32_16x16x64_i8 v[98:101], v[186:189], v[218:221], v[98:101]
	v_mfma_i32_16x16x64_i8 v[102:105], v[202:205], v[218:221], v[102:105]
	v_mfma_i32_16x16x64_i8 v[86:89], v[186:189], v[226:229], v[86:89]
	v_mfma_i32_16x16x64_i8 v[78:81], v[202:205], v[226:229], v[78:81]
	v_mfma_i32_16x16x64_i8 v[58:61], v[186:189], v[234:237], v[58:61]
	v_mfma_i32_16x16x64_i8 v[70:73], v[202:205], v[234:237], v[70:73]
	s_setprio 0
	s_barrier
	s_add_i32 s12, s12, s40
	v_lshl_add_u64 v[194:195], v[194:195], 0, s[24:25]
	s_mov_b32 m0, s12
	ds_read_b128 v[206:209], v200 offset:49152
	ds_read_b128 v[210:213], v200 offset:50176
	ds_read_b128 v[214:217], v200 offset:51200
	ds_read_b128 v[218:221], v200 offset:52224
	ds_read_b128 v[222:225], v200 offset:53248
	ds_read_b128 v[226:229], v200 offset:54272
	ds_read_b128 v[230:233], v200 offset:55296
	ds_read_b128 v[234:237], v200 offset:56320
	global_load_lds_dwordx4 v[194:195], off
	s_add_i32 m0, s12, 0x2000
	s_add_u32 s12, s36, 0x40080
	v_lshl_add_u64 v[194:195], v[238:239], 0, s[24:25]
	s_addc_u32 s13, s37, 0
	s_add_i32 s36, s64, s40
	global_load_lds_dwordx4 v[194:195], off
	v_lshl_add_u64 v[194:195], s[12:13], 0, v[148:149]
	s_mov_b32 m0, s36
	s_nop 0
	global_load_lds_dwordx4 v[194:195], off
	v_lshl_add_u64 v[194:195], s[12:13], 0, v[150:151]
	s_add_i32 m0, s36, 0x2000
	s_nop 0
	global_load_lds_dwordx4 v[194:195], off
	v_lshl_add_u64 v[194:195], v[240:241], 0, s[24:25]
	s_mov_b32 m0, s55
	s_nop 0
	global_load_lds_dwordx4 v[194:195], off
	v_lshl_add_u64 v[194:195], v[242:243], 0, s[24:25]
	s_mov_b32 m0, s56
	s_nop 0
	global_load_lds_dwordx4 v[194:195], off
	s_waitcnt vmcnt(8)
	s_waitcnt lgkmcnt(0)
	s_barrier
	s_setprio 1
	s_waitcnt lgkmcnt(0)
	v_mfma_i32_16x16x64_i8 v[54:57], v[106:109], v[206:209], v[54:57]
	v_mfma_i32_16x16x64_i8 v[50:53], v[114:117], v[206:209], v[50:53]
	v_mfma_i32_16x16x64_i8 v[34:37], v[106:109], v[214:217], v[34:37]
	v_mfma_i32_16x16x64_i8 v[38:41], v[114:117], v[214:217], v[38:41]
	v_mfma_i32_16x16x64_i8 v[22:25], v[106:109], v[222:225], v[22:25]
	v_mfma_i32_16x16x64_i8 v[18:21], v[114:117], v[222:225], v[18:21]
	v_mfma_i32_16x16x64_i8 v[2:5], v[106:109], v[230:233], v[2:5]
	v_mfma_i32_16x16x64_i8 v[6:9], v[114:117], v[230:233], v[6:9]
	v_mfma_i32_16x16x64_i8 v[54:57], v[110:113], v[210:213], v[54:57]
	v_mfma_i32_16x16x64_i8 v[50:53], v[118:121], v[210:213], v[50:53]
	v_mfma_i32_16x16x64_i8 v[34:37], v[110:113], v[218:221], v[34:37]
	v_mfma_i32_16x16x64_i8 v[38:41], v[118:121], v[218:221], v[38:41]
	v_mfma_i32_16x16x64_i8 v[22:25], v[110:113], v[226:229], v[22:25]
	v_mfma_i32_16x16x64_i8 v[18:21], v[118:121], v[226:229], v[18:21]
	v_mfma_i32_16x16x64_i8 v[2:5], v[110:113], v[234:237], v[2:5]
	v_mfma_i32_16x16x64_i8 v[6:9], v[118:121], v[234:237], v[6:9]
	s_setprio 0
	s_setprio 1
	v_mfma_i32_16x16x64_i8 v[66:69], v[182:185], v[206:209], v[66:69]
	v_mfma_i32_16x16x64_i8 v[62:65], v[190:193], v[206:209], v[62:65]
	v_mfma_i32_16x16x64_i8 v[42:45], v[182:185], v[214:217], v[42:45]
	v_mfma_i32_16x16x64_i8 v[46:49], v[190:193], v[214:217], v[46:49]
	v_mfma_i32_16x16x64_i8 v[30:33], v[182:185], v[222:225], v[30:33]
	v_mfma_i32_16x16x64_i8 v[26:29], v[190:193], v[222:225], v[26:29]
	v_mfma_i32_16x16x64_i8 v[10:13], v[182:185], v[230:233], v[10:13]
	v_mfma_i32_16x16x64_i8 v[14:17], v[190:193], v[230:233], v[14:17]
	v_mfma_i32_16x16x64_i8 v[66:69], v[186:189], v[210:213], v[66:69]
	v_mfma_i32_16x16x64_i8 v[62:65], v[202:205], v[210:213], v[62:65]
	v_mfma_i32_16x16x64_i8 v[42:45], v[186:189], v[218:221], v[42:45]
	v_mfma_i32_16x16x64_i8 v[46:49], v[202:205], v[218:221], v[46:49]
	v_mfma_i32_16x16x64_i8 v[30:33], v[186:189], v[226:229], v[30:33]
	v_mfma_i32_16x16x64_i8 v[26:29], v[202:205], v[226:229], v[26:29]
	v_mfma_i32_16x16x64_i8 v[10:13], v[186:189], v[234:237], v[10:13]
	v_mfma_i32_16x16x64_i8 v[14:17], v[202:205], v[234:237], v[14:17]
	s_setprio 0
	s_barrier
	s_add_i32 s63, s63, 2
	s_add_u32 s61, s61, 0x100
	s_addc_u32 s62, s62, 0
	s_cmp_gt_u32 s63, 13
	s_mov_b64 s[12:13], s[14:15]
	s_cbranch_scc0 .LBB0_246
	s_branch .Lpk1_exit

.Lpk1_exit:
	s_and_b64 vcc, s[4:5], exec
	v_readlane_b32 s60, v254, 32
	v_readlane_b32 s61, v254, 33
	v_readlane_b32 s62, v254, 34
	v_readlane_b32 s63, v254, 35
	v_readlane_b32 s64, v254, 36
	v_readlane_b32 s65, v254, 37
	v_readlane_b32 s66, v254, 38
	v_readlane_b32 s67, v254, 39
	v_readlane_b32 s68, v254, 40
	v_readlane_b32 s69, v254, 41
	v_readlane_b32 s70, v254, 42
	v_readlane_b32 s71, v254, 43
	v_readlane_b32 s72, v254, 44
	v_readlane_b32 s73, v254, 45
	v_readlane_b32 s74, v254, 46
	v_readlane_b32 s75, v254, 47
	s_cbranch_vccz .LBB0_253
	s_and_saveexec_b64 s[4:5], s[6:7]
	s_xor_b64 s[4:5], exec, s[4:5]
	s_lshl_b32 s12, s28, 8
	s_ashr_i32 s13, s12, 31
	v_lshl_add_u64 v[106:107], s[12:13], 2, v[168:169]
	s_movk_i32 s12, 0xfc00
	s_mov_b32 s13, -1
	v_lshl_add_u64 v[106:107], v[106:107], 0, s[12:13]
	s_andn2_saveexec_b64 s[4:5], s[4:5]
	s_lshl_b32 s12, s18, 8
	s_ashr_i32 s13, s12, 31
	v_lshl_add_u64 v[106:107], s[12:13], 2, v[170:171]
	s_or_b64 exec, exec, s[4:5]
	s_lshl_b32 s4, s59, 11
	s_and_b32 s4, s4, 0x800
	s_add_i32 m0, s41, s4
	s_nop 0
	global_load_lds_dword v[106:107], off

.LBB0_529:
	s_ashr_i32 s19, s18, 31
	s_lshl_b64 s[22:23], s[18:19], 18
	s_add_u32 s22, s38, s22
	s_addc_u32 s23, s39, s23
	s_and_b64 s[24:25], s[34:35], exec
	s_cselect_b32 s19, s23, s31
	s_cselect_b32 s53, s22, s30
	s_ashr_i32 s21, s20, 31
	s_lshl_b64 s[24:25], s[20:21], 18
	s_add_u32 s24, s40, s24
	s_addc_u32 s25, s41, s25
	s_and_b64 s[34:35], s[34:35], exec
	s_cselect_b32 s21, s25, s29
	s_cselect_b32 s54, s24, s28
	s_add_u32 s55, s28, 0x100
	s_addc_u32 s56, s29, 0
	s_mov_b32 s57, -2
	s_waitcnt lgkmcnt(0)
.Lpk2_entry:
	ds_read_b128 v[18:21], v195
	ds_read_b128 v[22:25], v195 offset:1024
	ds_read_b128 v[26:29], v195 offset:2048
	ds_read_b128 v[30:33], v195 offset:3072
	ds_read_b128 v[2:5], v196
	ds_read_b128 v[6:9], v196 offset:1024
	ds_read_b128 v[10:13], v196 offset:2048
	ds_read_b128 v[14:17], v196 offset:3072
	s_add_u32 s28, s30, 0x100
	s_addc_u32 s29, s31, 0
	s_cmp_eq_u32 s57, 4
	s_cselect_b32 s37, s19, s29
	s_cselect_b32 s36, s53, s28
	s_cselect_b32 s35, s21, s56
	s_cselect_b32 s34, s54, s55
	v_lshl_add_u64 v[222:223], s[30:31], 0, v[176:177]
	s_add_i32 m0, s27, 0xc000
	ds_read_b128 v[182:185], v197
	ds_read_b128 v[186:189], v197 offset:1024
	ds_read_b128 v[198:201], v197 offset:2048
	ds_read_b128 v[202:205], v197 offset:3072
	ds_read_b128 v[206:209], v197 offset:4096
	ds_read_b128 v[210:213], v197 offset:5120
	ds_read_b128 v[214:217], v197 offset:6144
	ds_read_b128 v[218:221], v197 offset:7168
	global_load_lds_dwordx4 v[222:223], off
	v_lshl_add_u64 v[222:223], s[30:31], 0, v[178:179]
	s_add_i32 m0, s27, 0xe000
	s_nop 0
	global_load_lds_dwordx4 v[222:223], off
	s_waitcnt vmcnt(8)
	s_waitcnt lgkmcnt(0)
	s_barrier
	s_setprio 1
	s_waitcnt lgkmcnt(0)
	v_mfma_f32_16x16x128_f8f6f4 v[158:161], v[18:25], v[182:189], 0
	v_mfma_f32_16x16x128_f8f6f4 v[154:157], v[26:33], v[182:189], 0
	v_mfma_f32_16x16x128_f8f6f4 v[138:141], v[18:25], v[198:205], 0
	v_mfma_f32_16x16x128_f8f6f4 v[142:145], v[26:33], v[198:205], 0
	v_mfma_f32_16x16x128_f8f6f4 v[126:129], v[18:25], v[206:213], 0
	v_mfma_f32_16x16x128_f8f6f4 v[122:125], v[26:33], v[206:213], 0
	v_mfma_f32_16x16x128_f8f6f4 v[106:109], v[18:25], v[214:221], 0
	v_mfma_f32_16x16x128_f8f6f4 v[110:113], v[26:33], v[214:221], 0
	s_setprio 0
	s_setprio 1
	v_mfma_f32_16x16x128_f8f6f4 v[150:153], v[2:9], v[182:189], 0
	v_mfma_f32_16x16x128_f8f6f4 v[146:149], v[10:17], v[182:189], 0
	v_mfma_f32_16x16x128_f8f6f4 v[130:133], v[2:9], v[198:205], 0
	v_mfma_f32_16x16x128_f8f6f4 v[134:137], v[10:17], v[198:205], 0
	v_mfma_f32_16x16x128_f8f6f4 v[118:121], v[2:9], v[206:213], 0
	v_mfma_f32_16x16x128_f8f6f4 v[114:117], v[10:17], v[206:213], 0
	v_mfma_f32_16x16x128_f8f6f4 v[98:101], v[2:9], v[214:221], 0
	v_mfma_f32_16x16x128_f8f6f4 v[102:105], v[10:17], v[214:221], 0
	s_setprio 0
	s_barrier
	s_add_i32 s30, s49, s42
	v_lshl_add_u64 v[182:183], s[34:35], 0, v[162:163]
	s_mov_b32 m0, s30
	ds_read_b128 v[198:201], v197 offset:16384
	ds_read_b128 v[202:205], v197 offset:17408
	ds_read_b128 v[206:209], v197 offset:18432
	ds_read_b128 v[210:213], v197 offset:19456
	ds_read_b128 v[214:217], v197 offset:20480
	ds_read_b128 v[218:221], v197 offset:21504
	ds_read_b128 v[222:225], v197 offset:22528
	ds_read_b128 v[226:229], v197 offset:23552
	global_load_lds_dwordx4 v[182:183], off
	s_add_i32 m0, s30, 0x2000
	s_add_u32 s30, s34, 0x20000
	v_lshl_add_u64 v[184:185], s[34:35], 0, v[164:165]
	s_addc_u32 s31, s35, 0
	s_add_i32 s58, s50, s42
	global_load_lds_dwordx4 v[184:185], off
	v_lshl_add_u64 v[186:187], s[30:31], 0, v[162:163]
	s_mov_b32 m0, s58
	v_lshl_add_u64 v[188:189], s[36:37], 0, v[168:169]
	global_load_lds_dwordx4 v[186:187], off
	v_lshl_add_u64 v[186:187], s[30:31], 0, v[164:165]
	s_add_i32 m0, s58, 0x2000
	s_nop 0
	global_load_lds_dwordx4 v[186:187], off
	v_lshl_add_u64 v[186:187], s[36:37], 0, v[166:167]
	s_mov_b32 m0, s27
	s_nop 0
	global_load_lds_dwordx4 v[186:187], off
	s_mov_b32 m0, s43
	s_nop 0
	global_load_lds_dwordx4 v[188:189], off
	s_waitcnt vmcnt(8)
	s_waitcnt lgkmcnt(0)
	s_barrier
	s_setprio 1
	s_waitcnt lgkmcnt(0)
	v_mfma_f32_16x16x128_f8f6f4 v[86:89], v[18:25], v[198:205], 0
	v_mfma_f32_16x16x128_f8f6f4 v[82:85], v[26:33], v[198:205], 0
	v_mfma_f32_16x16x128_f8f6f4 v[66:69], v[18:25], v[206:213], 0
	v_mfma_f32_16x16x128_f8f6f4 v[70:73], v[26:33], v[206:213], 0
	v_mfma_f32_16x16x128_f8f6f4 v[54:57], v[18:25], v[214:221], 0
	v_mfma_f32_16x16x128_f8f6f4 v[50:53], v[26:33], v[214:221], 0
	v_mfma_f32_16x16x128_f8f6f4 v[34:37], v[18:25], v[222:229], 0
	v_mfma_f32_16x16x128_f8f6f4 v[38:41], v[26:33], v[222:229], 0
	s_setprio 0
	s_setprio 1
	v_mfma_f32_16x16x128_f8f6f4 v[94:97], v[2:9], v[198:205], 0
	v_mfma_f32_16x16x128_f8f6f4 v[90:93], v[10:17], v[198:205], 0
	v_mfma_f32_16x16x128_f8f6f4 v[74:77], v[2:9], v[206:213], 0
	v_mfma_f32_16x16x128_f8f6f4 v[78:81], v[10:17], v[206:213], 0
	v_mfma_f32_16x16x128_f8f6f4 v[62:65], v[2:9], v[214:221], 0
	v_mfma_f32_16x16x128_f8f6f4 v[58:61], v[10:17], v[214:221], 0
	v_mfma_f32_16x16x128_f8f6f4 v[42:45], v[2:9], v[222:229], 0
	v_mfma_f32_16x16x128_f8f6f4 v[46:49], v[10:17], v[222:229], 0
	s_setprio 0
	s_barrier
	s_add_i32 s30, 0, 0x18000
	s_add_i32 s58, 0, 0x1c000
	v_add_u32_e32 v14, s30, v191
	v_add_u32_e32 v30, s58, v191
	ds_read_b128 v[2:5], v14
	ds_read_b128 v[6:9], v14 offset:1024
	ds_read_b128 v[10:13], v14 offset:2048
	ds_read_b128 v[14:17], v14 offset:3072
	ds_read_b128 v[18:21], v30
	ds_read_b128 v[22:25], v30 offset:1024
	ds_read_b128 v[26:29], v30 offset:2048
	ds_read_b128 v[30:33], v30 offset:3072
	s_mov_b32 m0, s44
	v_lshl_add_u64 v[230:231], s[36:37], 0, v[170:171]
	ds_read_b128 v[198:201], v197 offset:32768
	ds_read_b128 v[202:205], v197 offset:33792
	ds_read_b128 v[206:209], v197 offset:34816
	ds_read_b128 v[210:213], v197 offset:35840
	ds_read_b128 v[214:217], v197 offset:36864
	ds_read_b128 v[218:221], v197 offset:37888
	ds_read_b128 v[222:225], v197 offset:38912
	ds_read_b128 v[226:229], v197 offset:39936
	global_load_lds_dwordx4 v[230:231], off
	v_lshl_add_u64 v[230:231], s[36:37], 0, v[172:173]
	s_mov_b32 m0, s45
	s_nop 0
	global_load_lds_dwordx4 v[230:231], off
	s_waitcnt vmcnt(8)
	s_waitcnt lgkmcnt(0)
	s_barrier
	s_setprio 1
	s_waitcnt lgkmcnt(0)
	v_mfma_f32_16x16x128_f8f6f4 v[158:161], v[2:9], v[198:205], v[158:161]
	v_mfma_f32_16x16x128_f8f6f4 v[154:157], v[10:17], v[198:205], v[154:157]
	v_mfma_f32_16x16x128_f8f6f4 v[138:141], v[2:9], v[206:213], v[138:141]
	v_mfma_f32_16x16x128_f8f6f4 v[142:145], v[10:17], v[206:213], v[142:145]
	v_mfma_f32_16x16x128_f8f6f4 v[126:129], v[2:9], v[214:221], v[126:129]
	v_mfma_f32_16x16x128_f8f6f4 v[122:125], v[10:17], v[214:221], v[122:125]
	v_mfma_f32_16x16x128_f8f6f4 v[106:109], v[2:9], v[222:229], v[106:109]
	v_mfma_f32_16x16x128_f8f6f4 v[110:113], v[10:17], v[222:229], v[110:113]
	s_setprio 0
	s_setprio 1
	v_mfma_f32_16x16x128_f8f6f4 v[150:153], v[18:25], v[198:205], v[150:153]
	v_mfma_f32_16x16x128_f8f6f4 v[146:149], v[26:33], v[198:205], v[146:149]
	v_mfma_f32_16x16x128_f8f6f4 v[130:133], v[18:25], v[206:213], v[130:133]
	v_mfma_f32_16x16x128_f8f6f4 v[134:137], v[26:33], v[206:213], v[134:137]
	v_mfma_f32_16x16x128_f8f6f4 v[118:121], v[18:25], v[214:221], v[118:121]
	v_mfma_f32_16x16x128_f8f6f4 v[114:117], v[26:33], v[214:221], v[114:117]
	v_mfma_f32_16x16x128_f8f6f4 v[98:101], v[18:25], v[222:229], v[98:101]
	v_mfma_f32_16x16x128_f8f6f4 v[102:105], v[26:33], v[222:229], v[102:105]
	s_setprio 0
	s_barrier
	s_add_i32 s30, s30, s42
	v_lshl_add_u64 v[182:183], v[182:183], 0, s[10:11]
	s_mov_b32 m0, s30
	ds_read_b128 v[198:201], v197 offset:49152
	ds_read_b128 v[202:205], v197 offset:50176
	ds_read_b128 v[206:209], v197 offset:51200
	ds_read_b128 v[210:213], v197 offset:52224
	ds_read_b128 v[214:217], v197 offset:53248
	ds_read_b128 v[218:221], v197 offset:54272
	ds_read_b128 v[222:225], v197 offset:55296
	ds_read_b128 v[226:229], v197 offset:56320
	global_load_lds_dwordx4 v[182:183], off
	s_add_i32 m0, s30, 0x2000
	s_add_u32 s30, s34, 0x20080
	v_lshl_add_u64 v[182:183], v[184:185], 0, s[10:11]
	s_addc_u32 s31, s35, 0
	s_add_i32 s34, s58, s42
	global_load_lds_dwordx4 v[182:183], off
	v_lshl_add_u64 v[182:183], s[30:31], 0, v[162:163]
	s_mov_b32 m0, s34
	s_nop 0
	global_load_lds_dwordx4 v[182:183], off
	v_lshl_add_u64 v[182:183], s[30:31], 0, v[164:165]
	s_add_i32 m0, s34, 0x2000
	s_nop 0
	global_load_lds_dwordx4 v[182:183], off
	v_lshl_add_u64 v[182:183], v[186:187], 0, s[10:11]
	s_mov_b32 m0, s47
	s_nop 0
	global_load_lds_dwordx4 v[182:183], off
	v_lshl_add_u64 v[182:183], v[188:189], 0, s[10:11]
	s_mov_b32 m0, s48
	s_nop 0
	global_load_lds_dwordx4 v[182:183], off
	s_waitcnt vmcnt(8)
	s_waitcnt lgkmcnt(0)
	s_barrier
	s_setprio 1
	s_waitcnt lgkmcnt(0)
	v_mfma_f32_16x16x128_f8f6f4 v[86:89], v[2:9], v[198:205], v[86:89]
	v_mfma_f32_16x16x128_f8f6f4 v[82:85], v[10:17], v[198:205], v[82:85]
	v_mfma_f32_16x16x128_f8f6f4 v[66:69], v[2:9], v[206:213], v[66:69]
	v_mfma_f32_16x16x128_f8f6f4 v[70:73], v[10:17], v[206:213], v[70:73]
	v_mfma_f32_16x16x128_f8f6f4 v[54:57], v[2:9], v[214:221], v[54:57]
	v_mfma_f32_16x16x128_f8f6f4 v[50:53], v[10:17], v[214:221], v[50:53]
	v_mfma_f32_16x16x128_f8f6f4 v[34:37], v[2:9], v[222:229], v[34:37]
	v_mfma_f32_16x16x128_f8f6f4 v[38:41], v[10:17], v[222:229], v[38:41]
	s_setprio 0
	s_setprio 1
	v_mfma_f32_16x16x128_f8f6f4 v[94:97], v[18:25], v[198:205], v[94:97]
	v_mfma_f32_16x16x128_f8f6f4 v[90:93], v[26:33], v[198:205], v[90:93]
	v_mfma_f32_16x16x128_f8f6f4 v[74:77], v[18:25], v[206:213], v[74:77]
	v_mfma_f32_16x16x128_f8f6f4 v[78:81], v[26:33], v[206:213], v[78:81]
	v_mfma_f32_16x16x128_f8f6f4 v[62:65], v[18:25], v[214:221], v[62:65]
	v_mfma_f32_16x16x128_f8f6f4 v[58:61], v[26:33], v[214:221], v[58:61]
	v_mfma_f32_16x16x128_f8f6f4 v[42:45], v[18:25], v[222:229], v[42:45]
	v_mfma_f32_16x16x128_f8f6f4 v[46:49], v[26:33], v[222:229], v[46:49]
	s_setprio 0
	s_barrier
	s_add_i32 s57, s57, 2
	s_add_u32 s55, s55, 0x100
	s_addc_u32 s56, s56, 0
	s_cmp_gt_u32 s57, 5
	s_mov_b64 s[30:31], s[28:29]
	s_cbranch_scc0 .LBB0_530
	s_branch .Lpk2_exit

.Lpk2_exit:
	s_and_b64 vcc, exec, s[12:13]
	s_cbranch_vccz .LBB0_533
	s_barrier

.LBB0_553:
	s_ashr_i32 s19, s18, 31
	s_lshl_b64 s[22:23], s[18:19], 18
	s_add_u32 s22, s38, s22
	s_addc_u32 s23, s39, s23
	s_and_b64 s[24:25], s[34:35], exec
	s_cselect_b32 s19, s23, s29
	s_cselect_b32 s53, s22, s28
	s_ashr_i32 s21, s20, 31
	s_lshl_b64 s[24:25], s[20:21], 18
	s_add_u32 s24, s40, s24
	s_addc_u32 s25, s41, s25
	s_and_b64 s[34:35], s[34:35], exec
	s_cselect_b32 s21, s25, s31
	s_cselect_b32 s54, s24, s30
	s_add_u32 s55, s30, 0x100
	s_addc_u32 s56, s31, 0
	s_mov_b32 s57, -2
.Lpk3_entry:
	ds_read_b128 v[18:21], v197
	ds_read_b128 v[22:25], v197 offset:1024
	ds_read_b128 v[26:29], v197 offset:2048
	ds_read_b128 v[30:33], v197 offset:3072
	ds_read_b128 v[2:5], v198
	ds_read_b128 v[6:9], v198 offset:1024
	ds_read_b128 v[10:13], v198 offset:2048
	ds_read_b128 v[14:17], v198 offset:3072
	s_add_u32 s30, s28, 0x100
	s_addc_u32 s31, s29, 0
	s_cmp_eq_u32 s57, 4
	s_cselect_b32 s37, s19, s31
	s_cselect_b32 s36, s53, s30
	s_cselect_b32 s35, s21, s56
	s_cselect_b32 s34, s54, s55
	v_lshl_add_u64 v[224:225], s[28:29], 0, v[176:177]
	s_add_i32 m0, s27, 0xc000
	ds_read_b128 v[184:187], v199
	ds_read_b128 v[188:191], v199 offset:1024
	ds_read_b128 v[200:203], v199 offset:2048
	ds_read_b128 v[204:207], v199 offset:3072
	ds_read_b128 v[208:211], v199 offset:4096
	ds_read_b128 v[212:215], v199 offset:5120
	ds_read_b128 v[216:219], v199 offset:6144
	ds_read_b128 v[220:223], v199 offset:7168
	global_load_lds_dwordx4 v[224:225], off
	v_lshl_add_u64 v[224:225], s[28:29], 0, v[178:179]
	s_add_i32 m0, s27, 0xe000
	s_nop 0
	global_load_lds_dwordx4 v[224:225], off
	s_waitcnt vmcnt(8)
	s_waitcnt lgkmcnt(0)
	s_barrier
	s_setprio 1
	s_waitcnt lgkmcnt(0)
	v_mfma_f32_16x16x128_f8f6f4 v[158:161], v[18:25], v[184:191], 0
	v_mfma_f32_16x16x128_f8f6f4 v[154:157], v[26:33], v[184:191], 0
	v_mfma_f32_16x16x128_f8f6f4 v[138:141], v[18:25], v[200:207], 0
	v_mfma_f32_16x16x128_f8f6f4 v[142:145], v[26:33], v[200:207], 0
	v_mfma_f32_16x16x128_f8f6f4 v[126:129], v[18:25], v[208:215], 0
	v_mfma_f32_16x16x128_f8f6f4 v[122:125], v[26:33], v[208:215], 0
	v_mfma_f32_16x16x128_f8f6f4 v[106:109], v[18:25], v[216:223], 0
	v_mfma_f32_16x16x128_f8f6f4 v[110:113], v[26:33], v[216:223], 0
	s_setprio 0
	s_setprio 1
	v_mfma_f32_16x16x128_f8f6f4 v[150:153], v[2:9], v[184:191], 0
	v_mfma_f32_16x16x128_f8f6f4 v[146:149], v[10:17], v[184:191], 0
	v_mfma_f32_16x16x128_f8f6f4 v[130:133], v[2:9], v[200:207], 0
	v_mfma_f32_16x16x128_f8f6f4 v[134:137], v[10:17], v[200:207], 0
	v_mfma_f32_16x16x128_f8f6f4 v[118:121], v[2:9], v[208:215], 0
	v_mfma_f32_16x16x128_f8f6f4 v[114:117], v[10:17], v[208:215], 0
	v_mfma_f32_16x16x128_f8f6f4 v[98:101], v[2:9], v[216:223], 0
	v_mfma_f32_16x16x128_f8f6f4 v[102:105], v[10:17], v[216:223], 0
	s_setprio 0
	s_barrier
	s_add_i32 s28, s49, s42
	v_lshl_add_u64 v[184:185], s[34:35], 0, v[162:163]
	s_mov_b32 m0, s28
	ds_read_b128 v[200:203], v199 offset:16384
	ds_read_b128 v[204:207], v199 offset:17408
	ds_read_b128 v[208:211], v199 offset:18432
	ds_read_b128 v[212:215], v199 offset:19456
	ds_read_b128 v[216:219], v199 offset:20480
	ds_read_b128 v[220:223], v199 offset:21504
	ds_read_b128 v[224:227], v199 offset:22528
	ds_read_b128 v[228:231], v199 offset:23552
	global_load_lds_dwordx4 v[184:185], off
	s_add_i32 m0, s28, 0x2000
	s_add_u32 s28, s34, 0x20000
	v_lshl_add_u64 v[186:187], s[34:35], 0, v[164:165]
	s_addc_u32 s29, s35, 0
	s_add_i32 s58, s50, s42
	global_load_lds_dwordx4 v[186:187], off
	v_lshl_add_u64 v[188:189], s[28:29], 0, v[162:163]
	s_mov_b32 m0, s58
	v_lshl_add_u64 v[190:191], s[36:37], 0, v[168:169]
	global_load_lds_dwordx4 v[188:189], off
	v_lshl_add_u64 v[188:189], s[28:29], 0, v[164:165]
	s_add_i32 m0, s58, 0x2000
	s_nop 0
	global_load_lds_dwordx4 v[188:189], off
	v_lshl_add_u64 v[188:189], s[36:37], 0, v[166:167]
	s_mov_b32 m0, s27
	s_nop 0
	global_load_lds_dwordx4 v[188:189], off
	s_mov_b32 m0, s43
	s_nop 0
	global_load_lds_dwordx4 v[190:191], off
	s_waitcnt vmcnt(8)
	s_waitcnt lgkmcnt(0)
	s_barrier
	s_setprio 1
	s_waitcnt lgkmcnt(0)
	v_mfma_f32_16x16x128_f8f6f4 v[94:97], v[18:25], v[200:207], 0
	v_mfma_f32_16x16x128_f8f6f4 v[90:93], v[26:33], v[200:207], 0
	v_mfma_f32_16x16x128_f8f6f4 v[70:73], v[18:25], v[208:215], 0
	v_mfma_f32_16x16x128_f8f6f4 v[78:81], v[26:33], v[208:215], 0
	v_mfma_f32_16x16x128_f8f6f4 v[54:57], v[18:25], v[216:223], 0
	v_mfma_f32_16x16x128_f8f6f4 v[50:53], v[26:33], v[216:223], 0
	v_mfma_f32_16x16x128_f8f6f4 v[38:41], v[18:25], v[224:231], 0
	v_mfma_f32_16x16x128_f8f6f4 v[42:45], v[26:33], v[224:231], 0
	s_setprio 0
	s_setprio 1
	v_mfma_f32_16x16x128_f8f6f4 v[86:89], v[2:9], v[200:207], 0
	v_mfma_f32_16x16x128_f8f6f4 v[82:85], v[10:17], v[200:207], 0
	v_mfma_f32_16x16x128_f8f6f4 v[66:69], v[2:9], v[208:215], 0
	v_mfma_f32_16x16x128_f8f6f4 v[74:77], v[10:17], v[208:215], 0
	v_mfma_f32_16x16x128_f8f6f4 v[62:65], v[2:9], v[216:223], 0
	v_mfma_f32_16x16x128_f8f6f4 v[58:61], v[10:17], v[216:223], 0
	v_mfma_f32_16x16x128_f8f6f4 v[34:37], v[2:9], v[224:231], 0
	v_mfma_f32_16x16x128_f8f6f4 v[46:49], v[10:17], v[224:231], 0
	s_setprio 0
	s_barrier
	s_add_i32 s28, 0, 0x18000
	s_add_i32 s58, 0, 0x1c000
	v_add_u32_e32 v14, s28, v193
	v_add_u32_e32 v30, s58, v193
	ds_read_b128 v[2:5], v14
	ds_read_b128 v[6:9], v14 offset:1024
	ds_read_b128 v[10:13], v14 offset:2048
	ds_read_b128 v[14:17], v14 offset:3072
	ds_read_b128 v[18:21], v30
	ds_read_b128 v[22:25], v30 offset:1024
	ds_read_b128 v[26:29], v30 offset:2048
	ds_read_b128 v[30:33], v30 offset:3072
	s_mov_b32 m0, s44
	v_lshl_add_u64 v[232:233], s[36:37], 0, v[170:171]
	ds_read_b128 v[200:203], v199 offset:32768
	ds_read_b128 v[204:207], v199 offset:33792
	ds_read_b128 v[208:211], v199 offset:34816
	ds_read_b128 v[212:215], v199 offset:35840
	ds_read_b128 v[216:219], v199 offset:36864
	ds_read_b128 v[220:223], v199 offset:37888
	ds_read_b128 v[224:227], v199 offset:38912
	ds_read_b128 v[228:231], v199 offset:39936
	global_load_lds_dwordx4 v[232:233], off
	v_lshl_add_u64 v[232:233], s[36:37], 0, v[172:173]
	s_mov_b32 m0, s45
	s_nop 0
	global_load_lds_dwordx4 v[232:233], off
	s_waitcnt vmcnt(8)
	s_waitcnt lgkmcnt(0)
	s_barrier
	s_setprio 1
	s_waitcnt lgkmcnt(0)
	v_mfma_f32_16x16x128_f8f6f4 v[158:161], v[2:9], v[200:207], v[158:161]
	v_mfma_f32_16x16x128_f8f6f4 v[154:157], v[10:17], v[200:207], v[154:157]
	v_mfma_f32_16x16x128_f8f6f4 v[138:141], v[2:9], v[208:215], v[138:141]
	v_mfma_f32_16x16x128_f8f6f4 v[142:145], v[10:17], v[208:215], v[142:145]
	v_mfma_f32_16x16x128_f8f6f4 v[126:129], v[2:9], v[216:223], v[126:129]
	v_mfma_f32_16x16x128_f8f6f4 v[122:125], v[10:17], v[216:223], v[122:125]
	v_mfma_f32_16x16x128_f8f6f4 v[106:109], v[2:9], v[224:231], v[106:109]
	v_mfma_f32_16x16x128_f8f6f4 v[110:113], v[10:17], v[224:231], v[110:113]
	s_setprio 0
	s_setprio 1
	v_mfma_f32_16x16x128_f8f6f4 v[150:153], v[18:25], v[200:207], v[150:153]
	v_mfma_f32_16x16x128_f8f6f4 v[146:149], v[26:33], v[200:207], v[146:149]
	v_mfma_f32_16x16x128_f8f6f4 v[130:133], v[18:25], v[208:215], v[130:133]
	v_mfma_f32_16x16x128_f8f6f4 v[134:137], v[26:33], v[208:215], v[134:137]
	v_mfma_f32_16x16x128_f8f6f4 v[118:121], v[18:25], v[216:223], v[118:121]
	v_mfma_f32_16x16x128_f8f6f4 v[114:117], v[26:33], v[216:223], v[114:117]
	v_mfma_f32_16x16x128_f8f6f4 v[98:101], v[18:25], v[224:231], v[98:101]
	v_mfma_f32_16x16x128_f8f6f4 v[102:105], v[26:33], v[224:231], v[102:105]
	s_setprio 0
	s_barrier
	s_add_i32 s28, s28, s42
	v_lshl_add_u64 v[184:185], v[184:185], 0, s[10:11]
	s_mov_b32 m0, s28
	ds_read_b128 v[200:203], v199 offset:49152
	ds_read_b128 v[204:207], v199 offset:50176
	ds_read_b128 v[208:211], v199 offset:51200
	ds_read_b128 v[212:215], v199 offset:52224
	ds_read_b128 v[216:219], v199 offset:53248
	ds_read_b128 v[220:223], v199 offset:54272
	ds_read_b128 v[224:227], v199 offset:55296
	ds_read_b128 v[228:231], v199 offset:56320
	global_load_lds_dwordx4 v[184:185], off
	s_add_i32 m0, s28, 0x2000
	s_add_u32 s28, s34, 0x20080
	v_lshl_add_u64 v[184:185], v[186:187], 0, s[10:11]
	s_addc_u32 s29, s35, 0
	s_add_i32 s34, s58, s42
	global_load_lds_dwordx4 v[184:185], off
	v_lshl_add_u64 v[184:185], s[28:29], 0, v[162:163]
	s_mov_b32 m0, s34
	s_nop 0
	global_load_lds_dwordx4 v[184:185], off
	v_lshl_add_u64 v[184:185], s[28:29], 0, v[164:165]
	s_add_i32 m0, s34, 0x2000
	s_nop 0
	global_load_lds_dwordx4 v[184:185], off
	v_lshl_add_u64 v[184:185], v[188:189], 0, s[10:11]
	s_mov_b32 m0, s47
	s_nop 0
	global_load_lds_dwordx4 v[184:185], off
	v_lshl_add_u64 v[184:185], v[190:191], 0, s[10:11]
	s_mov_b32 m0, s48
	s_nop 0
	global_load_lds_dwordx4 v[184:185], off
	s_waitcnt vmcnt(8)
	s_waitcnt lgkmcnt(0)
	s_barrier
	s_setprio 1
	s_waitcnt lgkmcnt(0)
	v_mfma_f32_16x16x128_f8f6f4 v[94:97], v[2:9], v[200:207], v[94:97]
	v_mfma_f32_16x16x128_f8f6f4 v[90:93], v[10:17], v[200:207], v[90:93]
	v_mfma_f32_16x16x128_f8f6f4 v[70:73], v[2:9], v[208:215], v[70:73]
	v_mfma_f32_16x16x128_f8f6f4 v[78:81], v[10:17], v[208:215], v[78:81]
	v_mfma_f32_16x16x128_f8f6f4 v[54:57], v[2:9], v[216:223], v[54:57]
	v_mfma_f32_16x16x128_f8f6f4 v[50:53], v[10:17], v[216:223], v[50:53]
	v_mfma_f32_16x16x128_f8f6f4 v[38:41], v[2:9], v[224:231], v[38:41]
	v_mfma_f32_16x16x128_f8f6f4 v[42:45], v[10:17], v[224:231], v[42:45]
	s_setprio 0
	s_setprio 1
	v_mfma_f32_16x16x128_f8f6f4 v[86:89], v[18:25], v[200:207], v[86:89]
	v_mfma_f32_16x16x128_f8f6f4 v[82:85], v[26:33], v[200:207], v[82:85]
	v_mfma_f32_16x16x128_f8f6f4 v[66:69], v[18:25], v[208:215], v[66:69]
	v_mfma_f32_16x16x128_f8f6f4 v[74:77], v[26:33], v[208:215], v[74:77]
	v_mfma_f32_16x16x128_f8f6f4 v[62:65], v[18:25], v[216:223], v[62:65]
	v_mfma_f32_16x16x128_f8f6f4 v[58:61], v[26:33], v[216:223], v[58:61]
	v_mfma_f32_16x16x128_f8f6f4 v[34:37], v[18:25], v[224:231], v[34:37]
	v_mfma_f32_16x16x128_f8f6f4 v[46:49], v[26:33], v[224:231], v[46:49]
	s_setprio 0
	s_barrier
	s_add_i32 s57, s57, 2
	s_add_u32 s55, s55, 0x100
	s_addc_u32 s56, s56, 0
	s_cmp_gt_u32 s57, 5
	s_mov_b64 s[28:29], s[30:31]
	s_cbranch_scc0 .LBB0_554
	s_branch .Lpk3_exit

.LBB0_632:
	s_ashr_i32 s17, s16, 31
	s_lshl_b64 s[20:21], s[16:17], 19
	s_add_u32 s20, s13, s20
	s_addc_u32 s21, s15, s21
	s_and_b64 s[22:23], s[30:31], exec
	s_cselect_b32 s17, s21, s27
	s_cselect_b32 s49, s20, s26
	s_ashr_i32 s19, s18, 31
	s_lshl_b64 s[22:23], s[18:19], 19
	s_add_u32 s22, s36, s22
	s_addc_u32 s23, s37, s23
	s_and_b64 s[30:31], s[30:31], exec
	s_cselect_b32 s19, s23, s29
	s_cselect_b32 s50, s22, s28
	s_add_u32 s51, s28, 0x100
	s_addc_u32 s52, s29, 0
	s_mov_b32 s53, -2
.Lpk4_entry:
	ds_read_b128 v[18:21], v191
	ds_read_b128 v[22:25], v191 offset:1024
	ds_read_b128 v[26:29], v191 offset:2048
	ds_read_b128 v[30:33], v191 offset:3072
	ds_read_b128 v[2:5], v192
	ds_read_b128 v[6:9], v192 offset:1024
	ds_read_b128 v[10:13], v192 offset:2048
	ds_read_b128 v[14:17], v192 offset:3072
	s_add_u32 s28, s26, 0x100
	s_addc_u32 s29, s27, 0
	s_cmp_eq_u32 s53, 12
	s_cselect_b32 s35, s17, s29
	s_cselect_b32 s34, s49, s28
	s_cselect_b32 s31, s19, s52
	s_cselect_b32 s30, s50, s51
	v_lshl_add_u64 v[218:219], s[26:27], 0, v[172:173]
	s_add_i32 m0, s25, 0xc000
	ds_read_b128 v[180:183], v193
	ds_read_b128 v[184:187], v193 offset:1024
	ds_read_b128 v[194:197], v193 offset:2048
	ds_read_b128 v[198:201], v193 offset:3072
	ds_read_b128 v[202:205], v193 offset:4096
	ds_read_b128 v[206:209], v193 offset:5120
	ds_read_b128 v[210:213], v193 offset:6144
	ds_read_b128 v[214:217], v193 offset:7168
	global_load_lds_dwordx4 v[218:219], off
	v_lshl_add_u64 v[218:219], s[26:27], 0, v[174:175]
	s_add_i32 m0, s25, 0xe000
	s_nop 0
	global_load_lds_dwordx4 v[218:219], off
	s_waitcnt vmcnt(8)
	s_waitcnt lgkmcnt(0)
	s_barrier
	s_setprio 1
	s_waitcnt lgkmcnt(0)
	v_mfma_f32_16x16x128_f8f6f4 v[158:161], v[18:25], v[180:187], 0
	v_mfma_f32_16x16x128_f8f6f4 v[154:157], v[26:33], v[180:187], 0
	v_mfma_f32_16x16x128_f8f6f4 v[146:149], v[18:25], v[194:201], 0
	v_mfma_f32_16x16x128_f8f6f4 v[138:141], v[26:33], v[194:201], 0
	v_mfma_f32_16x16x128_f8f6f4 v[130:133], v[18:25], v[202:209], 0
	v_mfma_f32_16x16x128_f8f6f4 v[122:125], v[26:33], v[202:209], 0
	v_mfma_f32_16x16x128_f8f6f4 v[114:117], v[18:25], v[210:217], 0
	v_mfma_f32_16x16x128_f8f6f4 v[106:109], v[26:33], v[210:217], 0
	s_setprio 0
	s_setprio 1
	v_mfma_f32_16x16x128_f8f6f4 v[150:153], v[2:9], v[180:187], 0
	v_mfma_f32_16x16x128_f8f6f4 v[142:145], v[10:17], v[180:187], 0
	v_mfma_f32_16x16x128_f8f6f4 v[134:137], v[2:9], v[194:201], 0
	v_mfma_f32_16x16x128_f8f6f4 v[126:129], v[10:17], v[194:201], 0
	v_mfma_f32_16x16x128_f8f6f4 v[118:121], v[2:9], v[202:209], 0
	v_mfma_f32_16x16x128_f8f6f4 v[110:113], v[10:17], v[202:209], 0
	v_mfma_f32_16x16x128_f8f6f4 v[102:105], v[2:9], v[210:217], 0
	v_mfma_f32_16x16x128_f8f6f4 v[98:101], v[10:17], v[210:217], 0
	s_setprio 0
	s_barrier
	s_add_i32 s26, s46, s38
	v_lshl_add_u64 v[180:181], s[30:31], 0, v[162:163]
	s_mov_b32 m0, s26
	ds_read_b128 v[194:197], v193 offset:16384
	ds_read_b128 v[198:201], v193 offset:17408
	ds_read_b128 v[202:205], v193 offset:18432
	ds_read_b128 v[206:209], v193 offset:19456
	ds_read_b128 v[210:213], v193 offset:20480
	ds_read_b128 v[214:217], v193 offset:21504
	ds_read_b128 v[218:221], v193 offset:22528
	ds_read_b128 v[222:225], v193 offset:23552
	global_load_lds_dwordx4 v[180:181], off
	s_add_i32 m0, s26, 0x2000
	s_add_u32 s26, s30, 0x40000
	v_lshl_add_u64 v[182:183], s[30:31], 0, v[164:165]
	s_addc_u32 s27, s31, 0
	s_add_i32 s54, s47, s38
	global_load_lds_dwordx4 v[182:183], off
	v_lshl_add_u64 v[184:185], s[26:27], 0, v[162:163]
	s_mov_b32 m0, s54
	v_lshl_add_u64 v[186:187], s[34:35], 0, v[164:165]
	global_load_lds_dwordx4 v[184:185], off
	v_lshl_add_u64 v[184:185], s[26:27], 0, v[164:165]
	s_add_i32 m0, s54, 0x2000
	s_nop 0
	global_load_lds_dwordx4 v[184:185], off
	v_lshl_add_u64 v[184:185], s[34:35], 0, v[162:163]
	s_mov_b32 m0, s25
	s_nop 0
	global_load_lds_dwordx4 v[184:185], off
	s_mov_b32 m0, s39
	s_nop 0
	global_load_lds_dwordx4 v[186:187], off
	s_waitcnt vmcnt(8)
	s_waitcnt lgkmcnt(0)
	s_barrier
	s_setprio 1
	s_waitcnt lgkmcnt(0)
	v_mfma_f32_16x16x128_f8f6f4 v[86:89], v[18:25], v[194:201], 0
	v_mfma_f32_16x16x128_f8f6f4 v[82:85], v[26:33], v[194:201], 0
	v_mfma_f32_16x16x128_f8f6f4 v[70:73], v[18:25], v[202:209], 0
	v_mfma_f32_16x16x128_f8f6f4 v[66:69], v[26:33], v[202:209], 0
	v_mfma_f32_16x16x128_f8f6f4 v[54:57], v[18:25], v[210:217], 0
	v_mfma_f32_16x16x128_f8f6f4 v[50:53], v[26:33], v[210:217], 0
	v_mfma_f32_16x16x128_f8f6f4 v[38:41], v[18:25], v[218:225], 0
	v_mfma_f32_16x16x128_f8f6f4 v[34:37], v[26:33], v[218:225], 0
	s_setprio 0
	s_setprio 1
	v_mfma_f32_16x16x128_f8f6f4 v[94:97], v[2:9], v[194:201], 0
	v_mfma_f32_16x16x128_f8f6f4 v[90:93], v[10:17], v[194:201], 0
	v_mfma_f32_16x16x128_f8f6f4 v[78:81], v[2:9], v[202:209], 0
	v_mfma_f32_16x16x128_f8f6f4 v[74:77], v[10:17], v[202:209], 0
	v_mfma_f32_16x16x128_f8f6f4 v[62:65], v[2:9], v[210:217], 0
	v_mfma_f32_16x16x128_f8f6f4 v[58:61], v[10:17], v[210:217], 0
	v_mfma_f32_16x16x128_f8f6f4 v[46:49], v[2:9], v[218:225], 0
	v_mfma_f32_16x16x128_f8f6f4 v[42:45], v[10:17], v[218:225], 0
	s_setprio 0
	s_barrier
	s_add_i32 s26, 0, 0x18000
	s_add_i32 s54, 0, 0x1c000
	v_add_u32_e32 v14, s26, v189
	v_add_u32_e32 v30, s54, v189
	ds_read_b128 v[2:5], v14
	ds_read_b128 v[6:9], v14 offset:1024
	ds_read_b128 v[10:13], v14 offset:2048
	ds_read_b128 v[14:17], v14 offset:3072
	ds_read_b128 v[18:21], v30
	ds_read_b128 v[22:25], v30 offset:1024
	ds_read_b128 v[26:29], v30 offset:2048
	ds_read_b128 v[30:33], v30 offset:3072
	s_mov_b32 m0, s40
	v_lshl_add_u64 v[226:227], s[34:35], 0, v[166:167]
	ds_read_b128 v[194:197], v193 offset:32768
	ds_read_b128 v[198:201], v193 offset:33792
	ds_read_b128 v[202:205], v193 offset:34816
	ds_read_b128 v[206:209], v193 offset:35840
	ds_read_b128 v[210:213], v193 offset:36864
	ds_read_b128 v[214:217], v193 offset:37888
	ds_read_b128 v[218:221], v193 offset:38912
	ds_read_b128 v[222:225], v193 offset:39936
	global_load_lds_dwordx4 v[226:227], off
	v_lshl_add_u64 v[226:227], s[34:35], 0, v[168:169]
	s_mov_b32 m0, s41
	s_nop 0
	global_load_lds_dwordx4 v[226:227], off
	s_waitcnt vmcnt(8)
	s_waitcnt lgkmcnt(0)
	s_barrier
	s_setprio 1
	s_waitcnt lgkmcnt(0)
	v_mfma_f32_16x16x128_f8f6f4 v[158:161], v[2:9], v[194:201], v[158:161]
	v_mfma_f32_16x16x128_f8f6f4 v[154:157], v[10:17], v[194:201], v[154:157]
	v_mfma_f32_16x16x128_f8f6f4 v[146:149], v[2:9], v[202:209], v[146:149]
	v_mfma_f32_16x16x128_f8f6f4 v[138:141], v[10:17], v[202:209], v[138:141]
	v_mfma_f32_16x16x128_f8f6f4 v[130:133], v[2:9], v[210:217], v[130:133]
	v_mfma_f32_16x16x128_f8f6f4 v[122:125], v[10:17], v[210:217], v[122:125]
	v_mfma_f32_16x16x128_f8f6f4 v[114:117], v[2:9], v[218:225], v[114:117]
	v_mfma_f32_16x16x128_f8f6f4 v[106:109], v[10:17], v[218:225], v[106:109]
	s_setprio 0
	s_setprio 1
	v_mfma_f32_16x16x128_f8f6f4 v[150:153], v[18:25], v[194:201], v[150:153]
	v_mfma_f32_16x16x128_f8f6f4 v[142:145], v[26:33], v[194:201], v[142:145]
	v_mfma_f32_16x16x128_f8f6f4 v[134:137], v[18:25], v[202:209], v[134:137]
	v_mfma_f32_16x16x128_f8f6f4 v[126:129], v[26:33], v[202:209], v[126:129]
	v_mfma_f32_16x16x128_f8f6f4 v[118:121], v[18:25], v[210:217], v[118:121]
	v_mfma_f32_16x16x128_f8f6f4 v[110:113], v[26:33], v[210:217], v[110:113]
	v_mfma_f32_16x16x128_f8f6f4 v[102:105], v[18:25], v[218:225], v[102:105]
	v_mfma_f32_16x16x128_f8f6f4 v[98:101], v[26:33], v[218:225], v[98:101]
	s_setprio 0
	s_barrier
	s_add_i32 s26, s26, s38
	v_lshl_add_u64 v[180:181], v[180:181], 0, s[8:9]
	s_mov_b32 m0, s26
	ds_read_b128 v[194:197], v193 offset:49152
	ds_read_b128 v[198:201], v193 offset:50176
	ds_read_b128 v[202:205], v193 offset:51200
	ds_read_b128 v[206:209], v193 offset:52224
	ds_read_b128 v[210:213], v193 offset:53248
	ds_read_b128 v[214:217], v193 offset:54272
	ds_read_b128 v[218:221], v193 offset:55296
	ds_read_b128 v[222:225], v193 offset:56320
	global_load_lds_dwordx4 v[180:181], off
	s_add_i32 m0, s26, 0x2000
	s_add_u32 s26, s30, 0x40080
	v_lshl_add_u64 v[180:181], v[182:183], 0, s[8:9]
	s_addc_u32 s27, s31, 0
	s_add_i32 s30, s54, s38
	global_load_lds_dwordx4 v[180:181], off
	v_lshl_add_u64 v[180:181], s[26:27], 0, v[162:163]
	s_mov_b32 m0, s30
	s_nop 0
	global_load_lds_dwordx4 v[180:181], off
	v_lshl_add_u64 v[180:181], s[26:27], 0, v[164:165]
	s_add_i32 m0, s30, 0x2000
	s_nop 0
	global_load_lds_dwordx4 v[180:181], off
	v_lshl_add_u64 v[180:181], v[184:185], 0, s[8:9]
	s_mov_b32 m0, s44
	s_nop 0
	global_load_lds_dwordx4 v[180:181], off
	v_lshl_add_u64 v[180:181], v[186:187], 0, s[8:9]
	s_mov_b32 m0, s45
	s_nop 0
	global_load_lds_dwordx4 v[180:181], off
	s_waitcnt vmcnt(8)
	s_waitcnt lgkmcnt(0)
	s_barrier
	s_setprio 1
	s_waitcnt lgkmcnt(0)
	v_mfma_f32_16x16x128_f8f6f4 v[86:89], v[2:9], v[194:201], v[86:89]
	v_mfma_f32_16x16x128_f8f6f4 v[82:85], v[10:17], v[194:201], v[82:85]
	v_mfma_f32_16x16x128_f8f6f4 v[70:73], v[2:9], v[202:209], v[70:73]
	v_mfma_f32_16x16x128_f8f6f4 v[66:69], v[10:17], v[202:209], v[66:69]
	v_mfma_f32_16x16x128_f8f6f4 v[54:57], v[2:9], v[210:217], v[54:57]
	v_mfma_f32_16x16x128_f8f6f4 v[50:53], v[10:17], v[210:217], v[50:53]
	v_mfma_f32_16x16x128_f8f6f4 v[38:41], v[2:9], v[218:225], v[38:41]
	v_mfma_f32_16x16x128_f8f6f4 v[34:37], v[10:17], v[218:225], v[34:37]
	s_setprio 0
	s_setprio 1
	v_mfma_f32_16x16x128_f8f6f4 v[94:97], v[18:25], v[194:201], v[94:97]
	v_mfma_f32_16x16x128_f8f6f4 v[90:93], v[26:33], v[194:201], v[90:93]
	v_mfma_f32_16x16x128_f8f6f4 v[78:81], v[18:25], v[202:209], v[78:81]
	v_mfma_f32_16x16x128_f8f6f4 v[74:77], v[26:33], v[202:209], v[74:77]
	v_mfma_f32_16x16x128_f8f6f4 v[62:65], v[18:25], v[210:217], v[62:65]
	v_mfma_f32_16x16x128_f8f6f4 v[58:61], v[26:33], v[210:217], v[58:61]
	v_mfma_f32_16x16x128_f8f6f4 v[46:49], v[18:25], v[218:225], v[46:49]
	v_mfma_f32_16x16x128_f8f6f4 v[42:45], v[26:33], v[218:225], v[42:45]
	s_setprio 0
	s_barrier
	s_add_i32 s53, s53, 2
	s_add_u32 s51, s51, 0x100
	s_addc_u32 s52, s52, 0
	s_cmp_gt_u32 s53, 13
	s_mov_b64 s[26:27], s[28:29]
	s_cbranch_scc0 .LBB0_633
	s_branch .Lpk4_exit

.Lpk4_exit:
	s_and_b64 vcc, exec, s[10:11]
	s_cbranch_vccz .LBB0_636
	s_barrier

.LBB0_916:
	s_xor_b64 s[38:39], s[10:11], -1
	v_mov_b32_e32 v68, v67
	v_mov_b32_e32 v69, v67
	v_mov_b32_e32 v211, v67
	v_mov_b32_e32 v209, v67
	s_add_u32 s25, s8, 0x100
	v_mov_b32_e32 v66, v67
	s_addc_u32 s27, s9, 0
	v_lshl_add_u64 v[216:217], s[16:17], 0, v[210:211]
	v_lshl_add_u64 v[218:219], s[16:17], 0, v[208:209]
	s_mov_b32 s61, -2
	s_mov_b64 s[40:41], 0
	v_cndmask_b32_e64 v201, 0, 1, s[38:39]
	s_branch .Lpk5_entry
.Lpk5_entry:
	s_mov_b64 s[10:11], s[40:41]
	ds_read_b128 v[18:21], v232
	ds_read_b128 v[22:25], v232 offset:1024
	ds_read_b128 v[26:29], v232 offset:2048
	ds_read_b128 v[30:33], v232 offset:3072
	ds_read_b128 v[2:5], v233
	ds_read_b128 v[6:9], v233 offset:1024
	ds_read_b128 v[10:13], v233 offset:2048
	ds_read_b128 v[14:17], v233 offset:3072
	s_add_u32 s40, s10, 0x100
	s_addc_u32 s41, s11, 0
	s_add_u32 s44, s25, s10
	s_addc_u32 s45, s27, s11
	s_cmpk_eq_i32 s10, 0x700
	s_cselect_b64 s[8:9], -1, 0
	s_and_b64 s[42:43], s[8:9], exec
	s_cselect_b32 s63, 0, s40
	s_cselect_b32 s62, 0, s41
	s_cselect_b32 s43, s29, s45
	s_cselect_b32 s42, s28, s44
	s_add_u32 s44, s12, s63
	v_cndmask_b32_e64 v66, v214, v236, s[8:9]
	s_addc_u32 s45, s13, s62
	v_cndmask_b32_e64 v68, v212, v237, s[8:9]
	v_lshl_add_u64 v[220:221], v[216:217], 0, s[10:11]
	s_add_i32 m0, s35, 0xc000
	s_waitcnt lgkmcnt(0)
	ds_read_b128 v[34:37], v234
	ds_read_b128 v[38:41], v234 offset:1024
	ds_read_b128 v[42:45], v234 offset:2048
	ds_read_b128 v[46:49], v234 offset:3072
	ds_read_b128 v[50:53], v234 offset:4096
	ds_read_b128 v[54:57], v234 offset:5120
	ds_read_b128 v[58:61], v234 offset:6144
	ds_read_b128 v[62:65], v234 offset:7168
	global_load_lds_dwordx4 v[220:221], off
	v_lshl_add_u64 v[220:221], v[218:219], 0, s[10:11]
	s_add_i32 m0, s35, 0xe000
	s_nop 0
	global_load_lds_dwordx4 v[220:221], off
	s_waitcnt vmcnt(8)
	s_waitcnt lgkmcnt(0)
	s_barrier
	s_setprio 1
	s_waitcnt lgkmcnt(0)
	v_mfma_f32_16x16x128_f8f6f4 v[194:197], v[18:25], v[34:41], 0
	v_mfma_f32_16x16x128_f8f6f4 v[190:193], v[26:33], v[34:41], 0
	v_mfma_f32_16x16x128_f8f6f4 v[170:173], v[18:25], v[42:49], 0
	v_mfma_f32_16x16x128_f8f6f4 v[178:181], v[26:33], v[42:49], 0
	v_mfma_f32_16x16x128_f8f6f4 v[162:165], v[18:25], v[50:57], 0
	v_mfma_f32_16x16x128_f8f6f4 v[158:161], v[26:33], v[50:57], 0
	v_mfma_f32_16x16x128_f8f6f4 v[138:141], v[18:25], v[58:65], 0
	v_mfma_f32_16x16x128_f8f6f4 v[146:149], v[26:33], v[58:65], 0
	s_setprio 0
	s_setprio 1
	v_mfma_f32_16x16x128_f8f6f4 v[186:189], v[2:9], v[34:41], 0
	v_mfma_f32_16x16x128_f8f6f4 v[182:185], v[10:17], v[34:41], 0
	v_mfma_f32_16x16x128_f8f6f4 v[166:169], v[2:9], v[42:49], 0
	v_mfma_f32_16x16x128_f8f6f4 v[174:177], v[10:17], v[42:49], 0
	v_mfma_f32_16x16x128_f8f6f4 v[154:157], v[2:9], v[50:57], 0
	v_mfma_f32_16x16x128_f8f6f4 v[150:153], v[10:17], v[50:57], 0
	v_mfma_f32_16x16x128_f8f6f4 v[134:137], v[2:9], v[58:65], 0
	v_mfma_f32_16x16x128_f8f6f4 v[142:145], v[10:17], v[58:65], 0
	s_setprio 0
	s_barrier
	s_add_i32 s10, s54, s46
	v_lshl_add_u64 v[220:221], s[42:43], 0, v[198:199]
	s_mov_b32 m0, s10
	ds_read_b128 v[58:61], v234 offset:16384
	ds_read_b128 v[62:65], v234 offset:17408
	ds_read_b128 v[50:53], v234 offset:18432
	ds_read_b128 v[54:57], v234 offset:19456
	ds_read_b128 v[42:45], v234 offset:20480
	ds_read_b128 v[46:49], v234 offset:21504
	ds_read_b128 v[34:37], v234 offset:22528
	ds_read_b128 v[38:41], v234 offset:23552
	global_load_lds_dwordx4 v[220:221], off
	s_add_i32 m0, s10, 0x2000
	s_add_u32 s10, s42, 0x40000
	v_lshl_add_u64 v[222:223], s[42:43], 0, v[202:203]
	s_addc_u32 s11, s43, 0
	s_add_i32 s62, s55, s46
	global_load_lds_dwordx4 v[222:223], off
	v_lshl_add_u64 v[240:241], s[10:11], 0, v[198:199]
	s_mov_b32 m0, s62
	s_andn2_b64 vcc, exec, s[38:39]
	global_load_lds_dwordx4 v[240:241], off
	v_lshl_add_u64 v[240:241], s[10:11], 0, v[202:203]
	s_add_i32 m0, s62, 0x2000
	v_cmp_ne_u32_e64 s[10:11], 1, v201
	global_load_lds_dwordx4 v[240:241], off
	s_mov_b32 m0, s35
	s_nop 0
	global_load_lds_dwordx4 v66, s[44:45]
	s_mov_b32 m0, s48
	s_nop 0
	global_load_lds_dwordx4 v68, s[44:45]
	s_waitcnt vmcnt(8)
	s_waitcnt lgkmcnt(0)
	s_barrier
	s_cbranch_vccnz .Lpk5_hz
	s_setprio 1
	s_waitcnt lgkmcnt(0)
	v_mfma_f32_16x16x128_f8f6f4 v[130:133], v[18:25], v[58:65], 0
	v_mfma_f32_16x16x128_f8f6f4 v[126:129], v[26:33], v[58:65], 0
	v_mfma_f32_16x16x128_f8f6f4 v[106:109], v[18:25], v[50:57], 0
	v_mfma_f32_16x16x128_f8f6f4 v[114:117], v[26:33], v[50:57], 0
	v_mfma_f32_16x16x128_f8f6f4 v[98:101], v[18:25], v[42:49], 0
	v_mfma_f32_16x16x128_f8f6f4 v[90:93], v[26:33], v[42:49], 0
	v_mfma_f32_16x16x128_f8f6f4 v[70:73], v[18:25], v[34:41], 0
	v_mfma_f32_16x16x128_f8f6f4 v[78:81], v[26:33], v[34:41], 0
	s_setprio 0
	s_setprio 1
	v_mfma_f32_16x16x128_f8f6f4 v[122:125], v[2:9], v[58:65], 0
	v_mfma_f32_16x16x128_f8f6f4 v[118:121], v[10:17], v[58:65], 0
	v_mfma_f32_16x16x128_f8f6f4 v[102:105], v[2:9], v[50:57], 0
	v_mfma_f32_16x16x128_f8f6f4 v[110:113], v[10:17], v[50:57], 0
	v_mfma_f32_16x16x128_f8f6f4 v[94:97], v[2:9], v[42:49], 0
	v_mfma_f32_16x16x128_f8f6f4 v[86:89], v[10:17], v[42:49], 0
	v_mfma_f32_16x16x128_f8f6f4 v[74:77], v[2:9], v[34:41], 0
	v_mfma_f32_16x16x128_f8f6f4 v[82:85], v[10:17], v[34:41], 0
	s_setprio 0

.Lpk5_hz:
	v_mov_b64_e32 v[130:131], 0
	v_mov_b64_e32 v[132:133], 0
	v_mov_b64_e32 v[126:127], 0
	v_mov_b64_e32 v[128:129], 0
	v_mov_b64_e32 v[106:107], 0
	v_mov_b64_e32 v[108:109], 0
	v_mov_b64_e32 v[114:115], 0
	v_mov_b64_e32 v[116:117], 0
	v_mov_b64_e32 v[98:99], 0
	v_mov_b64_e32 v[100:101], 0
	v_mov_b64_e32 v[90:91], 0
	v_mov_b64_e32 v[92:93], 0
	v_mov_b64_e32 v[70:71], 0
	v_mov_b64_e32 v[72:73], 0
	v_mov_b64_e32 v[78:79], 0
	v_mov_b64_e32 v[80:81], 0
	v_mov_b64_e32 v[122:123], 0
	v_mov_b64_e32 v[124:125], 0
	v_mov_b64_e32 v[118:119], 0
	v_mov_b64_e32 v[120:121], 0
	v_mov_b64_e32 v[102:103], 0
	v_mov_b64_e32 v[104:105], 0
	v_mov_b64_e32 v[110:111], 0
	v_mov_b64_e32 v[112:113], 0
	v_mov_b64_e32 v[94:95], 0
	v_mov_b64_e32 v[96:97], 0
	v_mov_b64_e32 v[86:87], 0
	v_mov_b64_e32 v[88:89], 0
	v_mov_b64_e32 v[74:75], 0
	v_mov_b64_e32 v[76:77], 0
	v_mov_b64_e32 v[82:83], 0
	v_mov_b64_e32 v[84:85], 0
	s_branch .Lpk5_920

.LBB0_953:
	s_xor_b64 s[36:37], s[10:11], -1
	v_mov_b32_e32 v68, v67
	v_mov_b32_e32 v69, v67
	v_mov_b32_e32 v211, v67
	v_mov_b32_e32 v209, v67
	s_add_u32 s25, s8, 0x100
	v_mov_b32_e32 v66, v67
	s_addc_u32 s27, s9, 0
	v_lshl_add_u64 v[216:217], s[16:17], 0, v[210:211]
	v_lshl_add_u64 v[218:219], s[16:17], 0, v[208:209]
	s_mov_b32 s61, -2
	s_mov_b64 s[38:39], 0
	v_cndmask_b32_e64 v201, 0, 1, s[36:37]
	s_branch .Lpk6_entry
.Lpk6_entry:
	s_mov_b64 s[10:11], s[38:39]
	ds_read_b128 v[18:21], v232
	ds_read_b128 v[22:25], v232 offset:1024
	ds_read_b128 v[26:29], v232 offset:2048
	ds_read_b128 v[30:33], v232 offset:3072
	ds_read_b128 v[2:5], v233
	ds_read_b128 v[6:9], v233 offset:1024
	ds_read_b128 v[10:13], v233 offset:2048
	ds_read_b128 v[14:17], v233 offset:3072
	s_add_u32 s38, s10, 0x100
	s_addc_u32 s39, s11, 0
	s_add_u32 s42, s25, s10
	s_addc_u32 s43, s27, s11
	s_cmpk_eq_i32 s10, 0x700
	s_cselect_b64 s[8:9], -1, 0
	s_and_b64 s[40:41], s[8:9], exec
	s_cselect_b32 s63, 0, s38
	s_cselect_b32 s62, 0, s39
	s_cselect_b32 s41, s29, s43
	s_cselect_b32 s40, s28, s42
	s_add_u32 s42, s12, s63
	v_cndmask_b32_e64 v66, v214, v236, s[8:9]
	s_addc_u32 s43, s13, s62
	v_cndmask_b32_e64 v68, v212, v237, s[8:9]
	v_lshl_add_u64 v[220:221], v[216:217], 0, s[10:11]
	s_add_i32 m0, s31, 0xc000
	s_waitcnt lgkmcnt(0)
	ds_read_b128 v[34:37], v234
	ds_read_b128 v[38:41], v234 offset:1024
	ds_read_b128 v[42:45], v234 offset:2048
	ds_read_b128 v[46:49], v234 offset:3072
	ds_read_b128 v[50:53], v234 offset:4096
	ds_read_b128 v[54:57], v234 offset:5120
	ds_read_b128 v[58:61], v234 offset:6144
	ds_read_b128 v[62:65], v234 offset:7168
	global_load_lds_dwordx4 v[220:221], off
	v_lshl_add_u64 v[220:221], v[218:219], 0, s[10:11]
	s_add_i32 m0, s31, 0xe000
	s_nop 0
	global_load_lds_dwordx4 v[220:221], off
	s_waitcnt vmcnt(8)
	s_waitcnt lgkmcnt(0)
	s_barrier
	s_setprio 1
	s_waitcnt lgkmcnt(0)
	v_mfma_f32_16x16x128_f8f6f4 v[194:197], v[18:25], v[34:41], 0
	v_mfma_f32_16x16x128_f8f6f4 v[190:193], v[26:33], v[34:41], 0
	v_mfma_f32_16x16x128_f8f6f4 v[170:173], v[18:25], v[42:49], 0
	v_mfma_f32_16x16x128_f8f6f4 v[178:181], v[26:33], v[42:49], 0
	v_mfma_f32_16x16x128_f8f6f4 v[162:165], v[18:25], v[50:57], 0
	v_mfma_f32_16x16x128_f8f6f4 v[158:161], v[26:33], v[50:57], 0
	v_mfma_f32_16x16x128_f8f6f4 v[138:141], v[18:25], v[58:65], 0
	v_mfma_f32_16x16x128_f8f6f4 v[146:149], v[26:33], v[58:65], 0
	s_setprio 0
	s_setprio 1
	v_mfma_f32_16x16x128_f8f6f4 v[186:189], v[2:9], v[34:41], 0
	v_mfma_f32_16x16x128_f8f6f4 v[182:185], v[10:17], v[34:41], 0
	v_mfma_f32_16x16x128_f8f6f4 v[166:169], v[2:9], v[42:49], 0
	v_mfma_f32_16x16x128_f8f6f4 v[174:177], v[10:17], v[42:49], 0
	v_mfma_f32_16x16x128_f8f6f4 v[154:157], v[2:9], v[50:57], 0
	v_mfma_f32_16x16x128_f8f6f4 v[150:153], v[10:17], v[50:57], 0
	v_mfma_f32_16x16x128_f8f6f4 v[134:137], v[2:9], v[58:65], 0
	v_mfma_f32_16x16x128_f8f6f4 v[142:145], v[10:17], v[58:65], 0
	s_setprio 0
	s_barrier
	s_add_i32 s10, s52, s44
	v_lshl_add_u64 v[220:221], s[40:41], 0, v[202:203]
	s_mov_b32 m0, s10
	ds_read_b128 v[58:61], v234 offset:16384
	ds_read_b128 v[62:65], v234 offset:17408
	ds_read_b128 v[50:53], v234 offset:18432
	ds_read_b128 v[54:57], v234 offset:19456
	ds_read_b128 v[42:45], v234 offset:20480
	ds_read_b128 v[46:49], v234 offset:21504
	ds_read_b128 v[34:37], v234 offset:22528
	ds_read_b128 v[38:41], v234 offset:23552
	global_load_lds_dwordx4 v[220:221], off
	s_add_i32 m0, s10, 0x2000
	s_add_u32 s10, s40, 0x40000
	v_lshl_add_u64 v[222:223], s[40:41], 0, v[198:199]
	s_addc_u32 s11, s41, 0
	s_add_i32 s62, s53, s44
	global_load_lds_dwordx4 v[222:223], off
	v_lshl_add_u64 v[240:241], s[10:11], 0, v[202:203]
	s_mov_b32 m0, s62
	s_andn2_b64 vcc, exec, s[36:37]
	global_load_lds_dwordx4 v[240:241], off
	v_lshl_add_u64 v[240:241], s[10:11], 0, v[198:199]
	s_add_i32 m0, s62, 0x2000
	v_cmp_ne_u32_e64 s[10:11], 1, v201
	global_load_lds_dwordx4 v[240:241], off
	s_mov_b32 m0, s31
	s_nop 0
	global_load_lds_dwordx4 v66, s[42:43]
	s_mov_b32 m0, s46
	s_nop 0
	global_load_lds_dwordx4 v68, s[42:43]
	s_waitcnt vmcnt(8)
	s_waitcnt lgkmcnt(0)
	s_barrier
	s_cbranch_vccnz .Lpk6_hz
	s_setprio 1
	s_waitcnt lgkmcnt(0)
	v_mfma_f32_16x16x128_f8f6f4 v[130:133], v[18:25], v[58:65], 0
	v_mfma_f32_16x16x128_f8f6f4 v[126:129], v[26:33], v[58:65], 0
	v_mfma_f32_16x16x128_f8f6f4 v[106:109], v[18:25], v[50:57], 0
	v_mfma_f32_16x16x128_f8f6f4 v[114:117], v[26:33], v[50:57], 0
	v_mfma_f32_16x16x128_f8f6f4 v[98:101], v[18:25], v[42:49], 0
	v_mfma_f32_16x16x128_f8f6f4 v[90:93], v[26:33], v[42:49], 0
	v_mfma_f32_16x16x128_f8f6f4 v[70:73], v[18:25], v[34:41], 0
	v_mfma_f32_16x16x128_f8f6f4 v[78:81], v[26:33], v[34:41], 0
	s_setprio 0
	s_setprio 1
	v_mfma_f32_16x16x128_f8f6f4 v[122:125], v[2:9], v[58:65], 0
	v_mfma_f32_16x16x128_f8f6f4 v[118:121], v[10:17], v[58:65], 0
	v_mfma_f32_16x16x128_f8f6f4 v[102:105], v[2:9], v[50:57], 0
	v_mfma_f32_16x16x128_f8f6f4 v[110:113], v[10:17], v[50:57], 0
	v_mfma_f32_16x16x128_f8f6f4 v[94:97], v[2:9], v[42:49], 0
	v_mfma_f32_16x16x128_f8f6f4 v[86:89], v[10:17], v[42:49], 0
	v_mfma_f32_16x16x128_f8f6f4 v[74:77], v[2:9], v[34:41], 0
	v_mfma_f32_16x16x128_f8f6f4 v[82:85], v[10:17], v[34:41], 0
	s_setprio 0

.LBB0_1118:
	s_xor_b64 s[34:35], s[34:35], -1
	v_mov_b32_e32 v68, v66
	v_mov_b32_e32 v69, v66
	s_add_u32 s19, s8, 0x100
	v_mov_b32_e32 v67, v66
	s_addc_u32 s21, s9, 0
	s_mov_b32 s63, -2
	v_cndmask_b32_e64 v242, 0, 1, s[34:35]
	s_branch .Lpk7_entry
.Lpk7_entry:
	ds_read_b128 v[18:21], v239
	ds_read_b128 v[22:25], v239 offset:1024
	ds_read_b128 v[26:29], v239 offset:2048
	ds_read_b128 v[30:33], v239 offset:3072
	ds_read_b128 v[2:5], v240
	ds_read_b128 v[6:9], v240 offset:1024
	ds_read_b128 v[10:13], v240 offset:2048
	ds_read_b128 v[14:17], v240 offset:3072
	s_mov_b64 s[8:9], s[28:29]
	s_add_u32 s28, s8, 0x100
	s_addc_u32 s29, s9, 0
	s_cmp_eq_u32 s63, 12
	s_cselect_b32 s39, s23, s29
	s_cselect_b32 s38, s22, s28
	s_cselect_b32 s37, s25, s21
	s_cselect_b32 s36, s24, s19
	v_lshl_add_u64 v[68:69], s[8:9], 0, v[216:217]
	s_add_i32 m0, s27, 0xc000
	s_waitcnt lgkmcnt(0)
	ds_read_b128 v[34:37], v241
	ds_read_b128 v[38:41], v241 offset:1024
	ds_read_b128 v[42:45], v241 offset:2048
	ds_read_b128 v[46:49], v241 offset:3072
	ds_read_b128 v[50:53], v241 offset:4096
	ds_read_b128 v[54:57], v241 offset:5120
	ds_read_b128 v[58:61], v241 offset:6144
	ds_read_b128 v[62:65], v241 offset:7168
	global_load_lds_dwordx4 v[68:69], off
	v_lshl_add_u64 v[68:69], s[8:9], 0, v[218:219]
	s_add_i32 m0, s27, 0xe000
	s_nop 0
	global_load_lds_dwordx4 v[68:69], off
	s_waitcnt vmcnt(8)
	s_waitcnt lgkmcnt(0)
	s_barrier
	s_setprio 1
	s_waitcnt lgkmcnt(0)
	v_mfma_f32_16x16x128_f8f6f4 v[194:197], v[18:25], v[34:41], 0
	v_mfma_f32_16x16x128_f8f6f4 v[190:193], v[26:33], v[34:41], 0
	v_mfma_f32_16x16x128_f8f6f4 v[174:177], v[18:25], v[42:49], 0
	v_mfma_f32_16x16x128_f8f6f4 v[182:185], v[26:33], v[42:49], 0
	v_mfma_f32_16x16x128_f8f6f4 v[166:169], v[18:25], v[50:57], 0
	v_mfma_f32_16x16x128_f8f6f4 v[158:161], v[26:33], v[50:57], 0
	v_mfma_f32_16x16x128_f8f6f4 v[142:145], v[18:25], v[58:65], 0
	v_mfma_f32_16x16x128_f8f6f4 v[150:153], v[26:33], v[58:65], 0
	s_setprio 0
	s_setprio 1
	v_mfma_f32_16x16x128_f8f6f4 v[186:189], v[2:9], v[34:41], 0
	v_mfma_f32_16x16x128_f8f6f4 v[178:181], v[10:17], v[34:41], 0
	v_mfma_f32_16x16x128_f8f6f4 v[162:165], v[2:9], v[42:49], 0
	v_mfma_f32_16x16x128_f8f6f4 v[170:173], v[10:17], v[42:49], 0
	v_mfma_f32_16x16x128_f8f6f4 v[154:157], v[2:9], v[50:57], 0
	v_mfma_f32_16x16x128_f8f6f4 v[146:149], v[10:17], v[50:57], 0
	v_mfma_f32_16x16x128_f8f6f4 v[138:141], v[2:9], v[58:65], 0
	v_mfma_f32_16x16x128_f8f6f4 v[134:137], v[10:17], v[58:65], 0
	s_setprio 0
	s_barrier
	s_add_i32 s8, s54, s41
	v_lshl_add_u64 v[68:69], s[36:37], 0, v[202:203]
	s_mov_b32 m0, s8
	ds_read_b128 v[58:61], v241 offset:16384
	ds_read_b128 v[62:65], v241 offset:17408
	ds_read_b128 v[50:53], v241 offset:18432
	ds_read_b128 v[54:57], v241 offset:19456
	ds_read_b128 v[42:45], v241 offset:20480
	ds_read_b128 v[46:49], v241 offset:21504
	ds_read_b128 v[34:37], v241 offset:22528
	ds_read_b128 v[38:41], v241 offset:23552
	global_load_lds_dwordx4 v[68:69], off
	s_add_i32 m0, s8, 0x2000
	s_add_u32 s8, s36, 0x40000
	v_lshl_add_u64 v[220:221], s[36:37], 0, v[204:205]
	s_addc_u32 s9, s37, 0
	s_add_i32 s64, s55, s41
	global_load_lds_dwordx4 v[220:221], off
	v_lshl_add_u64 v[222:223], s[8:9], 0, v[202:203]
	s_mov_b32 m0, s64
	v_lshl_add_u64 v[224:225], s[38:39], 0, v[208:209]
	global_load_lds_dwordx4 v[222:223], off
	v_lshl_add_u64 v[222:223], s[8:9], 0, v[204:205]
	s_add_i32 m0, s64, 0x2000
	v_cmp_ne_u32_e64 s[8:9], 1, v242
	global_load_lds_dwordx4 v[222:223], off
	v_lshl_add_u64 v[222:223], s[38:39], 0, v[206:207]
	s_mov_b32 m0, s27
	s_andn2_b64 vcc, exec, s[34:35]
	global_load_lds_dwordx4 v[222:223], off
	s_mov_b32 m0, s47
	s_nop 0
	global_load_lds_dwordx4 v[224:225], off
	s_waitcnt vmcnt(8)
	s_waitcnt lgkmcnt(0)
	s_barrier
	s_cbranch_vccnz .Lpk7_hz
	s_setprio 1
	s_waitcnt lgkmcnt(0)
	v_mfma_f32_16x16x128_f8f6f4 v[130:133], v[18:25], v[58:65], 0
	v_mfma_f32_16x16x128_f8f6f4 v[126:129], v[26:33], v[58:65], 0
	v_mfma_f32_16x16x128_f8f6f4 v[110:113], v[18:25], v[50:57], 0
	v_mfma_f32_16x16x128_f8f6f4 v[114:117], v[26:33], v[50:57], 0
	v_mfma_f32_16x16x128_f8f6f4 v[98:101], v[18:25], v[42:49], 0
	v_mfma_f32_16x16x128_f8f6f4 v[90:93], v[26:33], v[42:49], 0
	v_mfma_f32_16x16x128_f8f6f4 v[78:81], v[18:25], v[34:41], 0
	v_mfma_f32_16x16x128_f8f6f4 v[82:85], v[26:33], v[34:41], 0
	s_setprio 0
	s_setprio 1
	v_mfma_f32_16x16x128_f8f6f4 v[122:125], v[2:9], v[58:65], 0
	v_mfma_f32_16x16x128_f8f6f4 v[118:121], v[10:17], v[58:65], 0
	v_mfma_f32_16x16x128_f8f6f4 v[102:105], v[2:9], v[50:57], 0
	v_mfma_f32_16x16x128_f8f6f4 v[106:109], v[10:17], v[50:57], 0
	v_mfma_f32_16x16x128_f8f6f4 v[94:97], v[2:9], v[42:49], 0
	v_mfma_f32_16x16x128_f8f6f4 v[86:89], v[10:17], v[42:49], 0
	v_mfma_f32_16x16x128_f8f6f4 v[70:73], v[2:9], v[34:41], 0
	v_mfma_f32_16x16x128_f8f6f4 v[74:77], v[10:17], v[34:41], 0
	s_setprio 0

.Lpk7_hz:
	v_mov_b64_e32 v[130:131], 0
	v_mov_b64_e32 v[132:133], 0
	v_mov_b64_e32 v[126:127], 0
	v_mov_b64_e32 v[128:129], 0
	v_mov_b64_e32 v[110:111], 0
	v_mov_b64_e32 v[112:113], 0
	v_mov_b64_e32 v[114:115], 0
	v_mov_b64_e32 v[116:117], 0
	v_mov_b64_e32 v[98:99], 0
	v_mov_b64_e32 v[100:101], 0
	v_mov_b64_e32 v[90:91], 0
	v_mov_b64_e32 v[92:93], 0
	v_mov_b64_e32 v[78:79], 0
	v_mov_b64_e32 v[80:81], 0
	v_mov_b64_e32 v[82:83], 0
	v_mov_b64_e32 v[84:85], 0
	v_mov_b64_e32 v[122:123], 0
	v_mov_b64_e32 v[124:125], 0
	v_mov_b64_e32 v[118:119], 0
	v_mov_b64_e32 v[120:121], 0
	v_mov_b64_e32 v[102:103], 0
	v_mov_b64_e32 v[104:105], 0
	v_mov_b64_e32 v[106:107], 0
	v_mov_b64_e32 v[108:109], 0
	v_mov_b64_e32 v[94:95], 0
	v_mov_b64_e32 v[96:97], 0
	v_mov_b64_e32 v[86:87], 0
	v_mov_b64_e32 v[88:89], 0
	v_mov_b64_e32 v[70:71], 0
	v_mov_b64_e32 v[72:73], 0
	v_mov_b64_e32 v[74:75], 0
	v_mov_b64_e32 v[76:77], 0
	s_branch .Lpk7_1122
